# combo + the two pre-barrier waits in each GEMM segment merged into one s_waitcnt
# baseline (speedup 1.0000x reference)
.LBB0_177:
	s_add_u32 s28, s4, s26
	s_addc_u32 s29, s5, s27
	s_add_u32 s30, s28, 0xe000100
	s_addc_u32 s31, s29, 0
	ds_read_b128 v[24:27], v252
	ds_read_b128 v[28:31], v253
	s_and_b64 s[28:29], s[34:35], exec
	ds_read_b128 v[16:19], v252 offset:2048
	ds_read_b128 v[20:23], v253 offset:2048
	s_cselect_b32 s29, s7, s31
	s_cselect_b32 s28, s6, s30
	s_add_u32 s61, s56, s26
	ds_read_b128 v[8:11], v252 offset:16384
	ds_read_b128 v[12:15], v253 offset:16384
	s_addc_u32 s62, s57, s27
	ds_read_b128 v[0:3], v252 offset:18432
	ds_read_b128 v[4:7], v253 offset:18432
	s_and_b64 s[30:31], s[34:35], exec
	s_cselect_b32 s31, s23, s62
	s_cselect_b32 s30, s22, s61
	s_add_u32 s61, s58, s26
	s_addc_u32 s62, s59, s27
	s_and_b64 s[34:35], s[34:35], exec
	s_cselect_b32 s35, s25, s62
	s_cselect_b32 s34, s24, s61
	s_add_u32 s100, s16, s26
	s_addc_u32 s101, s17, s27
	s_add_i32 m0, s37, 0xc000
	ds_read_b128 v[186:189], v206
	ds_read_b128 v[214:217], v206 offset:2048
	ds_read_b128 v[190:193], v207
	ds_read_b128 v[218:221], v207 offset:2048
	ds_read_b128 v[222:225], v206 offset:4096
	ds_read_b128 v[230:233], v206 offset:6144
	ds_read_b128 v[226:229], v207 offset:4096
	ds_read_b128 v[234:237], v207 offset:6144
	global_load_lds_dwordx4 v166, s[100:101]
	s_add_i32 m0, s37, 0xe000
	s_nop 0
	global_load_lds_dwordx4 v168, s[100:101]
	s_waitcnt vmcnt(8) lgkmcnt(0)
	s_setprio 1
	s_barrier
	s_cmp_eq_u32 s26, 0
	s_cbranch_scc1 .Lc0_P2_0
	v_mfma_f32_16x16x128_f8f6f4 v[156:159], v[24:31], v[186:193], v[156:159]
	v_mfma_f32_16x16x128_f8f6f4 v[152:155], v[16:23], v[186:193], v[152:155]
	v_mfma_f32_16x16x128_f8f6f4 v[136:139], v[16:23], v[214:221], v[136:139]
	v_mfma_f32_16x16x128_f8f6f4 v[144:147], v[24:31], v[214:221], v[144:147]
	v_mfma_f32_16x16x128_f8f6f4 v[128:131], v[24:31], v[222:229], v[128:131]
	v_mfma_f32_16x16x128_f8f6f4 v[120:123], v[16:23], v[222:229], v[120:123]
	v_mfma_f32_16x16x128_f8f6f4 v[104:107], v[16:23], v[230:237], v[104:107]
	v_mfma_f32_16x16x128_f8f6f4 v[112:115], v[24:31], v[230:237], v[112:115]
	v_mfma_f32_16x16x128_f8f6f4 v[148:151], v[8:15], v[186:193], v[148:151]
	v_mfma_f32_16x16x128_f8f6f4 v[140:143], v[0:7], v[186:193], v[140:143]
	v_mfma_f32_16x16x128_f8f6f4 v[124:127], v[0:7], v[214:221], v[124:127]
	v_mfma_f32_16x16x128_f8f6f4 v[132:135], v[8:15], v[214:221], v[132:135]
	v_mfma_f32_16x16x128_f8f6f4 v[116:119], v[8:15], v[222:229], v[116:119]
	v_mfma_f32_16x16x128_f8f6f4 v[108:111], v[0:7], v[222:229], v[108:111]
	v_mfma_f32_16x16x128_f8f6f4 v[96:99], v[0:7], v[230:237], v[96:99]
	v_mfma_f32_16x16x128_f8f6f4 v[100:103], v[8:15], v[230:237], v[100:103]
.Lc0b_P2_0:
	s_setprio 0
	s_barrier
	s_add_i32 s61, s44, s36
	s_mov_b32 m0, s61
	ds_read_b128 v[214:217], v206 offset:16384
	ds_read_b128 v[222:225], v206 offset:18432
	ds_read_b128 v[218:221], v207 offset:16384
	ds_read_b128 v[226:229], v207 offset:18432
	ds_read_b128 v[230:233], v206 offset:20480
	ds_read_b128 v[238:241], v206 offset:22528
	ds_read_b128 v[234:237], v207 offset:20480
	ds_read_b128 v[242:245], v207 offset:22528
	global_load_lds_dwordx4 v160, s[30:31]
	s_add_i32 m0, s61, 0x2000
	s_add_i32 s98, s46, s36
	global_load_lds_dwordx4 v162, s[30:31]
	s_mov_b32 m0, s98
	s_nop 0
	global_load_lds_dwordx4 v160, s[34:35]
	s_add_i32 m0, s98, 0x2000
	v_mov_b32_e32 v173, v165
	global_load_lds_dwordx4 v162, s[34:35]
	s_waitcnt vmcnt(6) lgkmcnt(0)
	s_setprio 1
	s_barrier
	s_cmp_eq_u32 s26, 0
	s_cbranch_scc1 .Lc0_P2_1
	v_mfma_f32_16x16x128_f8f6f4 v[92:95], v[24:31], v[214:221], v[92:95]
	v_mfma_f32_16x16x128_f8f6f4 v[88:91], v[16:23], v[214:221], v[88:91]
	v_mfma_f32_16x16x128_f8f6f4 v[72:75], v[16:23], v[222:229], v[72:75]
	v_mfma_f32_16x16x128_f8f6f4 v[80:83], v[24:31], v[222:229], v[80:83]
	s_mov_b32 m0, s37
	v_mfma_f32_16x16x128_f8f6f4 v[64:67], v[24:31], v[230:237], v[64:67]
	global_load_lds_dwordx4 v164, s[28:29]
	v_mfma_f32_16x16x128_f8f6f4 v[56:59], v[16:23], v[230:237], v[56:59]
	v_mfma_f32_16x16x128_f8f6f4 v[40:43], v[16:23], v[238:245], v[40:43]
	v_mfma_f32_16x16x128_f8f6f4 v[48:51], v[24:31], v[238:245], v[48:51]
	v_mfma_f32_16x16x128_f8f6f4 v[84:87], v[8:15], v[214:221], v[84:87]
	s_mov_b32 m0, s38
	v_mfma_f32_16x16x128_f8f6f4 v[76:79], v[0:7], v[214:221], v[76:79]
	global_load_lds_dwordx4 v172, s[28:29]
	v_mfma_f32_16x16x128_f8f6f4 v[60:63], v[0:7], v[222:229], v[60:63]
	v_mfma_f32_16x16x128_f8f6f4 v[68:71], v[8:15], v[222:229], v[68:71]
	v_mfma_f32_16x16x128_f8f6f4 v[52:55], v[8:15], v[230:237], v[52:55]
	v_mfma_f32_16x16x128_f8f6f4 v[44:47], v[0:7], v[230:237], v[44:47]
	v_mfma_f32_16x16x128_f8f6f4 v[32:35], v[0:7], v[238:245], v[32:35]
	v_mfma_f32_16x16x128_f8f6f4 v[36:39], v[8:15], v[238:245], v[36:39]
.Lc0b_P2_1:
	s_setprio 0
	s_barrier
	ds_read_b128 v[0:3], v252 offset:32768
	ds_read_b128 v[4:7], v253 offset:32768
	ds_read_b128 v[8:11], v252 offset:34816
	ds_read_b128 v[12:15], v253 offset:34816
	ds_read_b128 v[16:19], v252 offset:49152
	ds_read_b128 v[20:23], v253 offset:49152
	ds_read_b128 v[24:27], v252 offset:51200
	ds_read_b128 v[28:31], v253 offset:51200
	s_mov_b32 m0, s39
	ds_read_b128 v[214:217], v206 offset:32768
	ds_read_b128 v[222:225], v206 offset:34816
	ds_read_b128 v[218:221], v207 offset:32768
	ds_read_b128 v[226:229], v207 offset:34816
	ds_read_b128 v[230:233], v206 offset:36864
	ds_read_b128 v[238:241], v206 offset:38912
	ds_read_b128 v[234:237], v207 offset:36864
	ds_read_b128 v[242:245], v207 offset:38912
	global_load_lds_dwordx4 v184, s[28:29]
	s_mov_b32 m0, s40
	s_nop 0
	global_load_lds_dwordx4 v182, s[28:29]
	s_waitcnt vmcnt(8) lgkmcnt(0)
	s_setprio 1
	s_barrier
	v_mfma_f32_16x16x128_f8f6f4 v[156:159], v[0:7], v[214:221], v[156:159]
	v_mfma_f32_16x16x128_f8f6f4 v[152:155], v[8:15], v[214:221], v[152:155]
	v_mfma_f32_16x16x128_f8f6f4 v[136:139], v[8:15], v[222:229], v[136:139]
	v_mfma_f32_16x16x128_f8f6f4 v[144:147], v[0:7], v[222:229], v[144:147]
	v_mfma_f32_16x16x128_f8f6f4 v[128:131], v[0:7], v[230:237], v[128:131]
	v_mfma_f32_16x16x128_f8f6f4 v[120:123], v[8:15], v[230:237], v[120:123]
	v_mfma_f32_16x16x128_f8f6f4 v[104:107], v[8:15], v[238:245], v[104:107]
	v_mfma_f32_16x16x128_f8f6f4 v[112:115], v[0:7], v[238:245], v[112:115]
	v_mfma_f32_16x16x128_f8f6f4 v[148:151], v[16:23], v[214:221], v[148:151]
	v_mfma_f32_16x16x128_f8f6f4 v[140:143], v[24:31], v[214:221], v[140:143]
	v_mfma_f32_16x16x128_f8f6f4 v[124:127], v[24:31], v[222:229], v[124:127]
	v_mfma_f32_16x16x128_f8f6f4 v[132:135], v[16:23], v[222:229], v[132:135]
	v_mfma_f32_16x16x128_f8f6f4 v[116:119], v[16:23], v[230:237], v[116:119]
	v_mfma_f32_16x16x128_f8f6f4 v[108:111], v[24:31], v[230:237], v[108:111]
	v_mfma_f32_16x16x128_f8f6f4 v[96:99], v[24:31], v[238:245], v[96:99]
	v_mfma_f32_16x16x128_f8f6f4 v[100:103], v[16:23], v[238:245], v[100:103]
	s_setprio 0
	s_barrier
	s_add_i32 s99, s36, 0x17f80
	s_mov_b32 m0, s99
	ds_read_b128 v[214:217], v206 offset:49152
	ds_read_b128 v[222:225], v206 offset:51200
	ds_read_b128 v[218:221], v207 offset:49152
	ds_read_b128 v[226:229], v207 offset:51200
	ds_read_b128 v[230:233], v206 offset:53248
	ds_read_b128 v[238:241], v206 offset:55296
	ds_read_b128 v[234:237], v207 offset:53248
	ds_read_b128 v[242:245], v207 offset:55296
	global_load_lds_dwordx4 v160, s[30:31] offset:128
	s_add_i32 m0, s99, 0x2000
	s_add_i32 s99, s36, 0x1bf80
	global_load_lds_dwordx4 v162, s[30:31] offset:128
	s_mov_b32 m0, s99
	s_nop 0
	global_load_lds_dwordx4 v160, s[34:35] offset:128
	s_add_i32 m0, s99, 0x2000
	s_nop 0
	global_load_lds_dwordx4 v162, s[34:35] offset:128
	s_waitcnt vmcnt(6) lgkmcnt(0)
	s_setprio 1
	s_barrier
	v_mfma_f32_16x16x128_f8f6f4 v[92:95], v[0:7], v[214:221], v[92:95]
	v_mfma_f32_16x16x128_f8f6f4 v[88:91], v[8:15], v[214:221], v[88:91]
	v_mfma_f32_16x16x128_f8f6f4 v[72:75], v[8:15], v[222:229], v[72:75]
	v_mfma_f32_16x16x128_f8f6f4 v[80:83], v[0:7], v[222:229], v[80:83]
	s_add_i32 m0, s41, 0xffffff80
	v_mfma_f32_16x16x128_f8f6f4 v[64:67], v[0:7], v[230:237], v[64:67]
	global_load_lds_dwordx4 v164, s[28:29] offset:128
	v_mfma_f32_16x16x128_f8f6f4 v[56:59], v[8:15], v[230:237], v[56:59]
	v_mfma_f32_16x16x128_f8f6f4 v[40:43], v[8:15], v[238:245], v[40:43]
	v_mfma_f32_16x16x128_f8f6f4 v[48:51], v[0:7], v[238:245], v[48:51]
	v_mfma_f32_16x16x128_f8f6f4 v[84:87], v[16:23], v[214:221], v[84:87]
	s_add_i32 m0, s42, 0xffffff80
	v_mfma_f32_16x16x128_f8f6f4 v[76:79], v[24:31], v[214:221], v[76:79]
	global_load_lds_dwordx4 v172, s[28:29] offset:128
	v_mfma_f32_16x16x128_f8f6f4 v[60:63], v[24:31], v[222:229], v[60:63]
	v_mfma_f32_16x16x128_f8f6f4 v[68:71], v[16:23], v[222:229], v[68:71]
	v_mfma_f32_16x16x128_f8f6f4 v[52:55], v[16:23], v[230:237], v[52:55]
	v_mfma_f32_16x16x128_f8f6f4 v[44:47], v[24:31], v[230:237], v[44:47]
	v_mfma_f32_16x16x128_f8f6f4 v[32:35], v[24:31], v[238:245], v[32:35]
	v_mfma_f32_16x16x128_f8f6f4 v[36:39], v[16:23], v[238:245], v[36:39]
	s_setprio 0
	s_barrier
	s_add_i32 s60, s60, 2
	s_add_u32 s26, s26, 0x100
	s_addc_u32 s27, s27, 0
	s_cmp_gt_u32 s60, 5
	s_cbranch_scc1 .LBB0_180

.LBB0_430:
	s_add_u32 s26, s4, s24
	s_addc_u32 s27, s5, s25
	s_add_u32 s30, s26, 0x21c00100
	s_addc_u32 s31, s27, 0
	ds_read_b128 v[172:175], v252
	ds_read_b128 v[176:179], v253
	s_and_b64 s[26:27], s[28:29], exec
	ds_read_b128 v[180:183], v252 offset:2048
	ds_read_b128 v[184:187], v253 offset:2048
	s_cselect_b32 s27, s7, s31
	s_cselect_b32 s26, s6, s30
	s_add_u32 s65, s60, s24
	ds_read_b128 v[188:191], v252 offset:16384
	ds_read_b128 v[192:195], v253 offset:16384
	s_addc_u32 s66, s61, s25
	ds_read_b128 v[196:199], v252 offset:18432
	ds_read_b128 v[200:203], v253 offset:18432
	s_and_b64 s[30:31], s[28:29], exec
	s_cselect_b32 s31, s21, s66
	s_cselect_b32 s30, s20, s65
	s_add_u32 s65, s62, s24
	s_addc_u32 s66, s63, s25
	s_and_b64 s[28:29], s[28:29], exec
	s_cselect_b32 s29, s23, s66
	s_cselect_b32 s28, s22, s65
	v_lshl_add_u64 v[236:237], v[156:157], 0, s[24:25]
	s_add_i32 m0, s37, 0xc000
	ds_read_b128 v[204:207], v169
	ds_read_b128 v[208:211], v169 offset:1024
	ds_read_b128 v[212:215], v169 offset:2048
	ds_read_b128 v[216:219], v169 offset:3072
	ds_read_b128 v[220:223], v169 offset:4096
	ds_read_b128 v[224:227], v169 offset:5120
	ds_read_b128 v[228:231], v169 offset:6144
	ds_read_b128 v[232:235], v169 offset:7168
	global_load_lds_dwordx4 v[236:237], off
	v_lshl_add_u64 v[236:237], v[154:155], 0, s[24:25]
	s_add_i32 m0, s37, 0xe000
	s_nop 0
	global_load_lds_dwordx4 v[236:237], off
	s_waitcnt vmcnt(8) lgkmcnt(0)
	s_setprio 1
	s_barrier
	v_mfma_f32_16x16x32_bf16 v[140:143], v[172:175], v[204:207], v[140:143]
	v_mfma_f32_16x16x32_bf16 v[136:139], v[180:183], v[204:207], v[136:139]
	v_mfma_f32_16x16x32_bf16 v[124:127], v[172:175], v[212:215], v[124:127]
	v_mfma_f32_16x16x32_bf16 v[120:123], v[180:183], v[212:215], v[120:123]
	v_mfma_f32_16x16x32_bf16 v[92:95], v[172:175], v[220:223], v[92:95]
	v_mfma_f32_16x16x32_bf16 v[88:91], v[180:183], v[220:223], v[88:91]
	v_mfma_f32_16x16x32_bf16 v[76:79], v[172:175], v[228:231], v[76:79]
	v_mfma_f32_16x16x32_bf16 v[72:75], v[180:183], v[228:231], v[72:75]
	v_mfma_f32_16x16x32_bf16 v[140:143], v[176:179], v[208:211], v[140:143]
	v_mfma_f32_16x16x32_bf16 v[136:139], v[184:187], v[208:211], v[136:139]
	v_mfma_f32_16x16x32_bf16 v[124:127], v[176:179], v[216:219], v[124:127]
	v_mfma_f32_16x16x32_bf16 v[120:123], v[184:187], v[216:219], v[120:123]
	v_mfma_f32_16x16x32_bf16 v[92:95], v[176:179], v[224:227], v[92:95]
	v_mfma_f32_16x16x32_bf16 v[88:91], v[184:187], v[224:227], v[88:91]
	v_mfma_f32_16x16x32_bf16 v[76:79], v[176:179], v[232:235], v[76:79]
	v_mfma_f32_16x16x32_bf16 v[72:75], v[184:187], v[232:235], v[72:75]
	v_mfma_f32_16x16x32_bf16 v[132:135], v[188:191], v[204:207], v[132:135]
	v_mfma_f32_16x16x32_bf16 v[128:131], v[196:199], v[204:207], v[128:131]
	v_mfma_f32_16x16x32_bf16 v[108:111], v[188:191], v[212:215], v[108:111]
	v_mfma_f32_16x16x32_bf16 v[96:99], v[196:199], v[212:215], v[96:99]
	v_mfma_f32_16x16x32_bf16 v[84:87], v[188:191], v[220:223], v[84:87]
	v_mfma_f32_16x16x32_bf16 v[80:83], v[196:199], v[220:223], v[80:83]
	v_mfma_f32_16x16x32_bf16 v[68:71], v[188:191], v[228:231], v[68:71]
	v_mfma_f32_16x16x32_bf16 v[64:67], v[196:199], v[228:231], v[64:67]
	v_mfma_f32_16x16x32_bf16 v[132:135], v[192:195], v[208:211], v[132:135]
	v_mfma_f32_16x16x32_bf16 v[128:131], v[200:203], v[208:211], v[128:131]
	v_mfma_f32_16x16x32_bf16 v[108:111], v[192:195], v[216:219], v[108:111]
	v_mfma_f32_16x16x32_bf16 v[96:99], v[200:203], v[216:219], v[96:99]
	v_mfma_f32_16x16x32_bf16 v[84:87], v[192:195], v[224:227], v[84:87]
	v_mfma_f32_16x16x32_bf16 v[80:83], v[200:203], v[224:227], v[80:83]
	v_mfma_f32_16x16x32_bf16 v[68:71], v[192:195], v[232:235], v[68:71]
	v_mfma_f32_16x16x32_bf16 v[64:67], v[200:203], v[232:235], v[64:67]
	s_setprio 0
	s_barrier
	s_add_i32 s65, s48, s35
	v_lshl_add_u64 v[236:237], s[30:31], 0, v[146:147]
	s_mov_b32 m0, s65
	ds_read_b128 v[204:207], v169 offset:16384
	ds_read_b128 v[208:211], v169 offset:17408
	ds_read_b128 v[212:215], v169 offset:18432
	ds_read_b128 v[216:219], v169 offset:19456
	ds_read_b128 v[220:223], v169 offset:20480
	ds_read_b128 v[224:227], v169 offset:21504
	ds_read_b128 v[228:231], v169 offset:22528
	ds_read_b128 v[232:235], v169 offset:23552
	global_load_lds_dwordx4 v[236:237], off
	v_lshl_add_u64 v[238:239], s[30:31], 0, v[148:149]
	s_add_i32 m0, s65, 0x2000
	s_add_i32 s30, s50, s35
	global_load_lds_dwordx4 v[238:239], off
	v_lshl_add_u64 v[240:241], s[28:29], 0, v[146:147]
	s_mov_b32 m0, s30
	v_lshl_add_u64 v[242:243], s[28:29], 0, v[148:149]
	global_load_lds_dwordx4 v[240:241], off
	s_add_i32 m0, s30, 0x2000
	v_mov_b32_e32 v153, v151
	global_load_lds_dwordx4 v[242:243], off
	s_mov_b32 m0, s37
	v_lshl_add_u64 v[244:245], s[26:27], 0, v[150:151]
	global_load_lds_dwordx4 v150, s[26:27]
	s_mov_b32 m0, s38
	v_lshl_add_u64 v[246:247], s[26:27], 0, v[152:153]
	global_load_lds_dwordx4 v152, s[26:27]
	s_waitcnt vmcnt(8) lgkmcnt(0)
	s_setprio 1
	s_barrier
	v_mfma_f32_16x16x32_bf16 v[60:63], v[172:175], v[204:207], v[60:63]
	v_mfma_f32_16x16x32_bf16 v[56:59], v[180:183], v[204:207], v[56:59]
	v_mfma_f32_16x16x32_bf16 v[44:47], v[172:175], v[212:215], v[44:47]
	v_mfma_f32_16x16x32_bf16 v[40:43], v[180:183], v[212:215], v[40:43]
	v_mfma_f32_16x16x32_bf16 v[28:31], v[172:175], v[220:223], v[28:31]
	v_mfma_f32_16x16x32_bf16 v[24:27], v[180:183], v[220:223], v[24:27]
	v_mfma_f32_16x16x32_bf16 v[12:15], v[172:175], v[228:231], v[12:15]
	v_mfma_f32_16x16x32_bf16 v[8:11], v[180:183], v[228:231], v[8:11]
	v_mfma_f32_16x16x32_bf16 v[60:63], v[176:179], v[208:211], v[60:63]
	v_mfma_f32_16x16x32_bf16 v[56:59], v[184:187], v[208:211], v[56:59]
	v_mfma_f32_16x16x32_bf16 v[44:47], v[176:179], v[216:219], v[44:47]
	v_mfma_f32_16x16x32_bf16 v[40:43], v[184:187], v[216:219], v[40:43]
	v_mfma_f32_16x16x32_bf16 v[28:31], v[176:179], v[224:227], v[28:31]
	v_mfma_f32_16x16x32_bf16 v[24:27], v[184:187], v[224:227], v[24:27]
	v_mfma_f32_16x16x32_bf16 v[12:15], v[176:179], v[232:235], v[12:15]
	v_mfma_f32_16x16x32_bf16 v[8:11], v[184:187], v[232:235], v[8:11]
	v_mfma_f32_16x16x32_bf16 v[52:55], v[188:191], v[204:207], v[52:55]
	v_mfma_f32_16x16x32_bf16 v[48:51], v[196:199], v[204:207], v[48:51]
	v_mfma_f32_16x16x32_bf16 v[36:39], v[188:191], v[212:215], v[36:39]
	v_mfma_f32_16x16x32_bf16 v[32:35], v[196:199], v[212:215], v[32:35]
	v_mfma_f32_16x16x32_bf16 v[20:23], v[188:191], v[220:223], v[20:23]
	v_mfma_f32_16x16x32_bf16 v[16:19], v[196:199], v[220:223], v[16:19]
	v_mfma_f32_16x16x32_bf16 v[4:7], v[188:191], v[228:231], v[4:7]
	v_mfma_f32_16x16x32_bf16 v[0:3], v[196:199], v[228:231], v[0:3]
	v_mfma_f32_16x16x32_bf16 v[52:55], v[192:195], v[208:211], v[52:55]
	v_mfma_f32_16x16x32_bf16 v[48:51], v[200:203], v[208:211], v[48:51]
	v_mfma_f32_16x16x32_bf16 v[36:39], v[192:195], v[216:219], v[36:39]
	v_mfma_f32_16x16x32_bf16 v[32:35], v[200:203], v[216:219], v[32:35]
	v_mfma_f32_16x16x32_bf16 v[20:23], v[192:195], v[224:227], v[20:23]
	v_mfma_f32_16x16x32_bf16 v[16:19], v[200:203], v[224:227], v[16:19]
	v_mfma_f32_16x16x32_bf16 v[4:7], v[192:195], v[232:235], v[4:7]
	v_mfma_f32_16x16x32_bf16 v[0:3], v[200:203], v[232:235], v[0:3]
	s_setprio 0
	s_barrier
	s_add_i32 s28, 0, 0x18000
	ds_read_b128 v[172:175], v252 offset:32768
	ds_read_b128 v[176:179], v253 offset:32768
	s_add_i32 s29, 0, 0x1c000
	ds_read_b128 v[180:183], v252 offset:34816
	ds_read_b128 v[184:187], v253 offset:34816
	ds_read_b128 v[188:191], v252 offset:49152
	ds_read_b128 v[192:195], v253 offset:49152
	ds_read_b128 v[196:199], v252 offset:51200
	ds_read_b128 v[200:203], v253 offset:51200
	s_mov_b32 m0, s39
	v_lshl_add_u64 v[160:161], s[26:27], 0, v[160:161]
	ds_read_b128 v[204:207], v169 offset:32768
	ds_read_b128 v[208:211], v169 offset:33792
	ds_read_b128 v[212:215], v169 offset:34816
	ds_read_b128 v[216:219], v169 offset:35840
	ds_read_b128 v[220:223], v169 offset:36864
	ds_read_b128 v[224:227], v169 offset:37888
	ds_read_b128 v[228:231], v169 offset:38912
	ds_read_b128 v[232:235], v169 offset:39936
	global_load_lds_dwordx4 v[160:161], off
	v_lshl_add_u64 v[158:159], s[26:27], 0, v[158:159]
	s_mov_b32 m0, s40
	s_nop 0
	global_load_lds_dwordx4 v[158:159], off
	s_waitcnt vmcnt(8) lgkmcnt(0)
	s_setprio 1
	s_barrier
	v_mfma_f32_16x16x32_bf16 v[140:143], v[172:175], v[204:207], v[140:143]
	v_mfma_f32_16x16x32_bf16 v[136:139], v[180:183], v[204:207], v[136:139]
	v_mfma_f32_16x16x32_bf16 v[124:127], v[172:175], v[212:215], v[124:127]
	v_mfma_f32_16x16x32_bf16 v[120:123], v[180:183], v[212:215], v[120:123]
	v_mfma_f32_16x16x32_bf16 v[92:95], v[172:175], v[220:223], v[92:95]
	v_mfma_f32_16x16x32_bf16 v[88:91], v[180:183], v[220:223], v[88:91]
	v_mfma_f32_16x16x32_bf16 v[76:79], v[172:175], v[228:231], v[76:79]
	v_mfma_f32_16x16x32_bf16 v[72:75], v[180:183], v[228:231], v[72:75]
	v_mfma_f32_16x16x32_bf16 v[140:143], v[176:179], v[208:211], v[140:143]
	v_mfma_f32_16x16x32_bf16 v[136:139], v[184:187], v[208:211], v[136:139]
	v_mfma_f32_16x16x32_bf16 v[124:127], v[176:179], v[216:219], v[124:127]
	v_mfma_f32_16x16x32_bf16 v[120:123], v[184:187], v[216:219], v[120:123]
	v_mfma_f32_16x16x32_bf16 v[92:95], v[176:179], v[224:227], v[92:95]
	v_mfma_f32_16x16x32_bf16 v[88:91], v[184:187], v[224:227], v[88:91]
	v_mfma_f32_16x16x32_bf16 v[76:79], v[176:179], v[232:235], v[76:79]
	v_mfma_f32_16x16x32_bf16 v[72:75], v[184:187], v[232:235], v[72:75]
	v_mfma_f32_16x16x32_bf16 v[132:135], v[188:191], v[204:207], v[132:135]
	v_mfma_f32_16x16x32_bf16 v[128:131], v[196:199], v[204:207], v[128:131]
	v_mfma_f32_16x16x32_bf16 v[108:111], v[188:191], v[212:215], v[108:111]
	v_mfma_f32_16x16x32_bf16 v[96:99], v[196:199], v[212:215], v[96:99]
	v_mfma_f32_16x16x32_bf16 v[84:87], v[188:191], v[220:223], v[84:87]
	v_mfma_f32_16x16x32_bf16 v[80:83], v[196:199], v[220:223], v[80:83]
	v_mfma_f32_16x16x32_bf16 v[68:71], v[188:191], v[228:231], v[68:71]
	v_mfma_f32_16x16x32_bf16 v[64:67], v[196:199], v[228:231], v[64:67]
	v_mfma_f32_16x16x32_bf16 v[132:135], v[192:195], v[208:211], v[132:135]
	v_mfma_f32_16x16x32_bf16 v[128:131], v[200:203], v[208:211], v[128:131]
	v_mfma_f32_16x16x32_bf16 v[108:111], v[192:195], v[216:219], v[108:111]
	v_mfma_f32_16x16x32_bf16 v[96:99], v[200:203], v[216:219], v[96:99]
	v_mfma_f32_16x16x32_bf16 v[84:87], v[192:195], v[224:227], v[84:87]
	v_mfma_f32_16x16x32_bf16 v[80:83], v[200:203], v[224:227], v[80:83]
	v_mfma_f32_16x16x32_bf16 v[68:71], v[192:195], v[232:235], v[68:71]
	v_mfma_f32_16x16x32_bf16 v[64:67], v[200:203], v[232:235], v[64:67]
	s_setprio 0
	s_barrier
	s_add_i32 s26, s28, s35
	v_lshl_add_u64 v[232:233], v[236:237], 0, s[14:15]
	s_mov_b32 m0, s26
	ds_read_b128 v[158:161], v169 offset:49152
	ds_read_b128 v[204:207], v169 offset:50176
	ds_read_b128 v[208:211], v169 offset:51200
	ds_read_b128 v[212:215], v169 offset:52224
	ds_read_b128 v[216:219], v169 offset:53248
	ds_read_b128 v[220:223], v169 offset:54272
	ds_read_b128 v[224:227], v169 offset:55296
	ds_read_b128 v[228:231], v169 offset:56320
	global_load_lds_dwordx4 v[232:233], off
	v_lshl_add_u64 v[232:233], v[238:239], 0, s[14:15]
	s_add_i32 m0, s26, 0x2000
	s_add_i32 s26, s29, s35
	global_load_lds_dwordx4 v[232:233], off
	v_lshl_add_u64 v[232:233], v[240:241], 0, s[14:15]
	s_mov_b32 m0, s26
	s_nop 0
	global_load_lds_dwordx4 v[232:233], off
	v_lshl_add_u64 v[232:233], v[242:243], 0, s[14:15]
	s_add_i32 m0, s26, 0x2000
	s_nop 0
	global_load_lds_dwordx4 v[232:233], off
	v_lshl_add_u64 v[232:233], v[244:245], 0, s[14:15]
	s_mov_b32 m0, s45
	s_nop 0
	global_load_lds_dwordx4 v[232:233], off
	v_lshl_add_u64 v[232:233], v[246:247], 0, s[14:15]
	s_mov_b32 m0, s46
	s_nop 0
	global_load_lds_dwordx4 v[232:233], off
	s_waitcnt vmcnt(8) lgkmcnt(0)
	s_setprio 1
	s_barrier
	v_mfma_f32_16x16x32_bf16 v[60:63], v[172:175], v[158:161], v[60:63]
	v_mfma_f32_16x16x32_bf16 v[56:59], v[180:183], v[158:161], v[56:59]
	v_mfma_f32_16x16x32_bf16 v[44:47], v[172:175], v[208:211], v[44:47]
	v_mfma_f32_16x16x32_bf16 v[40:43], v[180:183], v[208:211], v[40:43]
	v_mfma_f32_16x16x32_bf16 v[28:31], v[172:175], v[216:219], v[28:31]
	v_mfma_f32_16x16x32_bf16 v[24:27], v[180:183], v[216:219], v[24:27]
	v_mfma_f32_16x16x32_bf16 v[12:15], v[172:175], v[224:227], v[12:15]
	v_mfma_f32_16x16x32_bf16 v[8:11], v[180:183], v[224:227], v[8:11]
	v_mfma_f32_16x16x32_bf16 v[60:63], v[176:179], v[204:207], v[60:63]
	v_mfma_f32_16x16x32_bf16 v[56:59], v[184:187], v[204:207], v[56:59]
	v_mfma_f32_16x16x32_bf16 v[44:47], v[176:179], v[212:215], v[44:47]
	v_mfma_f32_16x16x32_bf16 v[40:43], v[184:187], v[212:215], v[40:43]
	v_mfma_f32_16x16x32_bf16 v[28:31], v[176:179], v[220:223], v[28:31]
	v_mfma_f32_16x16x32_bf16 v[24:27], v[184:187], v[220:223], v[24:27]
	v_mfma_f32_16x16x32_bf16 v[12:15], v[176:179], v[228:231], v[12:15]
	v_mfma_f32_16x16x32_bf16 v[8:11], v[184:187], v[228:231], v[8:11]
	v_mfma_f32_16x16x32_bf16 v[52:55], v[188:191], v[158:161], v[52:55]
	v_mfma_f32_16x16x32_bf16 v[48:51], v[196:199], v[158:161], v[48:51]
	v_mfma_f32_16x16x32_bf16 v[36:39], v[188:191], v[208:211], v[36:39]
	v_mfma_f32_16x16x32_bf16 v[32:35], v[196:199], v[208:211], v[32:35]
	v_mfma_f32_16x16x32_bf16 v[20:23], v[188:191], v[216:219], v[20:23]
	v_mfma_f32_16x16x32_bf16 v[16:19], v[196:199], v[216:219], v[16:19]
	v_mfma_f32_16x16x32_bf16 v[4:7], v[188:191], v[224:227], v[4:7]
	v_mfma_f32_16x16x32_bf16 v[0:3], v[196:199], v[224:227], v[0:3]
	v_mfma_f32_16x16x32_bf16 v[52:55], v[192:195], v[204:207], v[52:55]
	v_mfma_f32_16x16x32_bf16 v[48:51], v[200:203], v[204:207], v[48:51]
	v_mfma_f32_16x16x32_bf16 v[36:39], v[192:195], v[212:215], v[36:39]
	v_mfma_f32_16x16x32_bf16 v[32:35], v[200:203], v[212:215], v[32:35]
	v_mfma_f32_16x16x32_bf16 v[20:23], v[192:195], v[220:223], v[20:23]
	v_mfma_f32_16x16x32_bf16 v[16:19], v[200:203], v[220:223], v[16:19]
	v_mfma_f32_16x16x32_bf16 v[4:7], v[192:195], v[228:231], v[4:7]
	v_mfma_f32_16x16x32_bf16 v[0:3], v[200:203], v[228:231], v[0:3]
	s_setprio 0
	s_barrier
	s_add_i32 s64, s64, 2
	s_add_u32 s24, s24, 0x100
	s_addc_u32 s25, s25, 0
	s_cmp_gt_u32 s64, 9
	s_cbranch_scc1 .LBB0_433

.LBB0_590:
	s_add_u32 s36, s8, s4
	s_addc_u32 s37, s9, s5
	s_add_u32 s38, s36, 0xe000100
	s_addc_u32 s39, s37, 0
	ds_read_b128 v[24:27], v252
	ds_read_b128 v[28:31], v253
	s_and_b64 s[36:37], s[40:41], exec
	ds_read_b128 v[16:19], v252 offset:2048
	ds_read_b128 v[20:23], v253 offset:2048
	s_cselect_b32 s37, s11, s39
	s_cselect_b32 s36, s10, s38
	s_add_u32 s90, s27, s4
	ds_read_b128 v[8:11], v252 offset:16384
	ds_read_b128 v[12:15], v253 offset:16384
	s_addc_u32 s91, s86, s5
	ds_read_b128 v[0:3], v252 offset:18432
	ds_read_b128 v[4:7], v253 offset:18432
	s_and_b64 s[38:39], s[40:41], exec
	s_cselect_b32 s39, s29, s91
	s_cselect_b32 s38, s28, s90
	s_add_u32 s90, s87, s4
	s_addc_u32 s91, s88, s5
	s_and_b64 s[40:41], s[40:41], exec
	s_cselect_b32 s41, s31, s91
	s_cselect_b32 s40, s30, s90
	s_add_u32 s100, s18, s4
	s_addc_u32 s101, s19, s5
	s_add_i32 m0, s61, 0xc000
	ds_read_b128 v[182:185], v201
	ds_read_b128 v[210:213], v201 offset:2048
	ds_read_b128 v[186:189], v202
	ds_read_b128 v[214:217], v202 offset:2048
	ds_read_b128 v[218:221], v201 offset:4096
	ds_read_b128 v[226:229], v201 offset:6144
	ds_read_b128 v[222:225], v202 offset:4096
	ds_read_b128 v[230:233], v202 offset:6144
	global_load_lds_dwordx4 v170, s[100:101]
	s_add_i32 m0, s61, 0xe000
	s_nop 0
	global_load_lds_dwordx4 v168, s[100:101]
	s_waitcnt vmcnt(8) lgkmcnt(0)
	s_setprio 1
	s_barrier
	s_cmp_eq_u32 s4, 0
	s_cbranch_scc1 .Lc0_P6_0
	v_mfma_f32_16x16x128_f8f6f4 v[156:159], v[24:31], v[182:189], v[156:159]
	v_mfma_f32_16x16x128_f8f6f4 v[148:151], v[16:23], v[182:189], v[148:151]
	v_mfma_f32_16x16x128_f8f6f4 v[132:135], v[16:23], v[210:217], v[132:135]
	v_mfma_f32_16x16x128_f8f6f4 v[140:143], v[24:31], v[210:217], v[140:143]
	v_mfma_f32_16x16x128_f8f6f4 v[124:127], v[24:31], v[218:225], v[124:127]
	v_mfma_f32_16x16x128_f8f6f4 v[116:119], v[16:23], v[218:225], v[116:119]
	v_mfma_f32_16x16x128_f8f6f4 v[100:103], v[16:23], v[226:233], v[100:103]
	v_mfma_f32_16x16x128_f8f6f4 v[108:111], v[24:31], v[226:233], v[108:111]
	v_mfma_f32_16x16x128_f8f6f4 v[152:155], v[8:15], v[182:189], v[152:155]
	v_mfma_f32_16x16x128_f8f6f4 v[144:147], v[0:7], v[182:189], v[144:147]
	v_mfma_f32_16x16x128_f8f6f4 v[128:131], v[0:7], v[210:217], v[128:131]
	v_mfma_f32_16x16x128_f8f6f4 v[136:139], v[8:15], v[210:217], v[136:139]
	v_mfma_f32_16x16x128_f8f6f4 v[120:123], v[8:15], v[218:225], v[120:123]
	v_mfma_f32_16x16x128_f8f6f4 v[112:115], v[0:7], v[218:225], v[112:115]
	v_mfma_f32_16x16x128_f8f6f4 v[96:99], v[0:7], v[226:233], v[96:99]
	v_mfma_f32_16x16x128_f8f6f4 v[104:107], v[8:15], v[226:233], v[104:107]
.Lc0b_P6_0:
	s_setprio 0
	s_barrier
	s_add_i32 s90, s72, s44
	s_mov_b32 m0, s90
	ds_read_b128 v[210:213], v201 offset:16384
	ds_read_b128 v[218:221], v201 offset:18432
	ds_read_b128 v[214:217], v202 offset:16384
	ds_read_b128 v[222:225], v202 offset:18432
	ds_read_b128 v[226:229], v201 offset:20480
	ds_read_b128 v[234:237], v201 offset:22528
	ds_read_b128 v[230:233], v202 offset:20480
	ds_read_b128 v[238:241], v202 offset:22528
	global_load_lds_dwordx4 v160, s[38:39]
	s_add_i32 m0, s90, 0x2000
	s_add_i32 s98, s74, s44
	global_load_lds_dwordx4 v162, s[38:39]
	s_mov_b32 m0, s98
	s_nop 0
	global_load_lds_dwordx4 v160, s[40:41]
	s_add_i32 m0, s98, 0x2000
	v_mov_b32_e32 v167, v165
	global_load_lds_dwordx4 v162, s[40:41]
	s_waitcnt vmcnt(6) lgkmcnt(0)
	s_setprio 1
	s_barrier
	s_cmp_eq_u32 s4, 0
	s_cbranch_scc1 .Lc0_P6_1
	v_mfma_f32_16x16x128_f8f6f4 v[92:95], v[24:31], v[210:217], v[92:95]
	v_mfma_f32_16x16x128_f8f6f4 v[84:87], v[16:23], v[210:217], v[84:87]
	v_mfma_f32_16x16x128_f8f6f4 v[68:71], v[16:23], v[218:225], v[68:71]
	v_mfma_f32_16x16x128_f8f6f4 v[76:79], v[24:31], v[218:225], v[76:79]
	s_mov_b32 m0, s61
	v_mfma_f32_16x16x128_f8f6f4 v[60:63], v[24:31], v[226:233], v[60:63]
	global_load_lds_dwordx4 v164, s[36:37]
	v_mfma_f32_16x16x128_f8f6f4 v[52:55], v[16:23], v[226:233], v[52:55]
	v_mfma_f32_16x16x128_f8f6f4 v[36:39], v[16:23], v[234:241], v[36:39]
	v_mfma_f32_16x16x128_f8f6f4 v[44:47], v[24:31], v[234:241], v[44:47]
	v_mfma_f32_16x16x128_f8f6f4 v[88:91], v[8:15], v[210:217], v[88:91]
	s_mov_b32 m0, s62
	v_mfma_f32_16x16x128_f8f6f4 v[80:83], v[0:7], v[210:217], v[80:83]
	global_load_lds_dwordx4 v166, s[36:37]
	v_mfma_f32_16x16x128_f8f6f4 v[64:67], v[0:7], v[218:225], v[64:67]
	v_mfma_f32_16x16x128_f8f6f4 v[72:75], v[8:15], v[218:225], v[72:75]
	v_mfma_f32_16x16x128_f8f6f4 v[56:59], v[8:15], v[226:233], v[56:59]
	v_mfma_f32_16x16x128_f8f6f4 v[48:51], v[0:7], v[226:233], v[48:51]
	v_mfma_f32_16x16x128_f8f6f4 v[32:35], v[0:7], v[234:241], v[32:35]
	v_mfma_f32_16x16x128_f8f6f4 v[40:43], v[8:15], v[234:241], v[40:43]
.Lc0b_P6_1:
	s_setprio 0
	s_barrier
	ds_read_b128 v[0:3], v252 offset:32768
	ds_read_b128 v[4:7], v253 offset:32768
	ds_read_b128 v[8:11], v252 offset:34816
	ds_read_b128 v[12:15], v253 offset:34816
	ds_read_b128 v[16:19], v252 offset:49152
	ds_read_b128 v[20:23], v253 offset:49152
	ds_read_b128 v[24:27], v252 offset:51200
	ds_read_b128 v[28:31], v253 offset:51200
	s_mov_b32 m0, s63
	ds_read_b128 v[210:213], v201 offset:32768
	ds_read_b128 v[218:221], v201 offset:34816
	ds_read_b128 v[214:217], v202 offset:32768
	ds_read_b128 v[222:225], v202 offset:34816
	ds_read_b128 v[226:229], v201 offset:36864
	ds_read_b128 v[234:237], v201 offset:38912
	ds_read_b128 v[230:233], v202 offset:36864
	ds_read_b128 v[238:241], v202 offset:38912
	global_load_lds_dwordx4 v180, s[36:37]
	s_mov_b32 m0, s64
	s_nop 0
	global_load_lds_dwordx4 v178, s[36:37]
	s_waitcnt vmcnt(8) lgkmcnt(0)
	s_setprio 1
	s_barrier
	v_mfma_f32_16x16x128_f8f6f4 v[156:159], v[0:7], v[210:217], v[156:159]
	v_mfma_f32_16x16x128_f8f6f4 v[148:151], v[8:15], v[210:217], v[148:151]
	v_mfma_f32_16x16x128_f8f6f4 v[132:135], v[8:15], v[218:225], v[132:135]
	v_mfma_f32_16x16x128_f8f6f4 v[140:143], v[0:7], v[218:225], v[140:143]
	v_mfma_f32_16x16x128_f8f6f4 v[124:127], v[0:7], v[226:233], v[124:127]
	v_mfma_f32_16x16x128_f8f6f4 v[116:119], v[8:15], v[226:233], v[116:119]
	v_mfma_f32_16x16x128_f8f6f4 v[100:103], v[8:15], v[234:241], v[100:103]
	v_mfma_f32_16x16x128_f8f6f4 v[108:111], v[0:7], v[234:241], v[108:111]
	v_mfma_f32_16x16x128_f8f6f4 v[152:155], v[16:23], v[210:217], v[152:155]
	v_mfma_f32_16x16x128_f8f6f4 v[144:147], v[24:31], v[210:217], v[144:147]
	v_mfma_f32_16x16x128_f8f6f4 v[128:131], v[24:31], v[218:225], v[128:131]
	v_mfma_f32_16x16x128_f8f6f4 v[136:139], v[16:23], v[218:225], v[136:139]
	v_mfma_f32_16x16x128_f8f6f4 v[120:123], v[16:23], v[226:233], v[120:123]
	v_mfma_f32_16x16x128_f8f6f4 v[112:115], v[24:31], v[226:233], v[112:115]
	v_mfma_f32_16x16x128_f8f6f4 v[96:99], v[24:31], v[234:241], v[96:99]
	v_mfma_f32_16x16x128_f8f6f4 v[104:107], v[16:23], v[234:241], v[104:107]
	s_setprio 0
	s_barrier
	s_add_i32 s99, s44, 0x17f80
	s_mov_b32 m0, s99
	ds_read_b128 v[210:213], v201 offset:49152
	ds_read_b128 v[218:221], v201 offset:51200
	ds_read_b128 v[214:217], v202 offset:49152
	ds_read_b128 v[222:225], v202 offset:51200
	ds_read_b128 v[226:229], v201 offset:53248
	ds_read_b128 v[234:237], v201 offset:55296
	ds_read_b128 v[230:233], v202 offset:53248
	ds_read_b128 v[238:241], v202 offset:55296
	global_load_lds_dwordx4 v160, s[38:39] offset:128
	s_add_i32 m0, s99, 0x2000
	s_add_i32 s99, s44, 0x1bf80
	global_load_lds_dwordx4 v162, s[38:39] offset:128
	s_mov_b32 m0, s99
	s_nop 0
	global_load_lds_dwordx4 v160, s[40:41] offset:128
	s_add_i32 m0, s99, 0x2000
	s_nop 0
	global_load_lds_dwordx4 v162, s[40:41] offset:128
	s_waitcnt vmcnt(6) lgkmcnt(0)
	s_setprio 1
	s_barrier
	v_mfma_f32_16x16x128_f8f6f4 v[92:95], v[0:7], v[210:217], v[92:95]
	v_mfma_f32_16x16x128_f8f6f4 v[84:87], v[8:15], v[210:217], v[84:87]
	v_mfma_f32_16x16x128_f8f6f4 v[68:71], v[8:15], v[218:225], v[68:71]
	v_mfma_f32_16x16x128_f8f6f4 v[76:79], v[0:7], v[218:225], v[76:79]
	s_add_i32 m0, s65, 0xffffff80
	v_mfma_f32_16x16x128_f8f6f4 v[60:63], v[0:7], v[226:233], v[60:63]
	global_load_lds_dwordx4 v164, s[36:37] offset:128
	v_mfma_f32_16x16x128_f8f6f4 v[52:55], v[8:15], v[226:233], v[52:55]
	v_mfma_f32_16x16x128_f8f6f4 v[36:39], v[8:15], v[234:241], v[36:39]
	v_mfma_f32_16x16x128_f8f6f4 v[44:47], v[0:7], v[234:241], v[44:47]
	v_mfma_f32_16x16x128_f8f6f4 v[88:91], v[16:23], v[210:217], v[88:91]
	s_add_i32 m0, s66, 0xffffff80
	v_mfma_f32_16x16x128_f8f6f4 v[80:83], v[24:31], v[210:217], v[80:83]
	global_load_lds_dwordx4 v166, s[36:37] offset:128
	v_mfma_f32_16x16x128_f8f6f4 v[64:67], v[24:31], v[218:225], v[64:67]
	v_mfma_f32_16x16x128_f8f6f4 v[72:75], v[16:23], v[218:225], v[72:75]
	v_mfma_f32_16x16x128_f8f6f4 v[56:59], v[16:23], v[226:233], v[56:59]
	v_mfma_f32_16x16x128_f8f6f4 v[48:51], v[24:31], v[226:233], v[48:51]
	v_mfma_f32_16x16x128_f8f6f4 v[32:35], v[24:31], v[234:241], v[32:35]
	v_mfma_f32_16x16x128_f8f6f4 v[40:43], v[16:23], v[234:241], v[40:43]
	s_setprio 0
	s_barrier
	s_add_i32 s89, s89, 2
	s_add_u32 s4, s4, 0x100
	s_addc_u32 s5, s5, 0
	s_cmp_gt_u32 s89, 5
	s_cbranch_scc1 .LBB0_593

.LBB0_672:
	s_add_u32 s36, s6, s34
	s_addc_u32 s37, s7, s35
	s_add_u32 s38, s36, 0x12c00100
	s_addc_u32 s39, s37, 0
	ds_read_b128 v[24:27], v252
	ds_read_b128 v[28:31], v253
	s_and_b64 s[36:37], s[40:41], exec
	ds_read_b128 v[16:19], v252 offset:2048
	ds_read_b128 v[20:23], v253 offset:2048
	s_cselect_b32 s37, s9, s39
	s_cselect_b32 s36, s8, s38
	s_add_u32 s86, s27, s34
	ds_read_b128 v[8:11], v252 offset:16384
	ds_read_b128 v[12:15], v253 offset:16384
	s_addc_u32 s87, s82, s35
	ds_read_b128 v[0:3], v252 offset:18432
	ds_read_b128 v[4:7], v253 offset:18432
	s_and_b64 s[38:39], s[40:41], exec
	s_cselect_b32 s39, s29, s87
	s_cselect_b32 s38, s28, s86
	s_add_u32 s86, s83, s34
	s_addc_u32 s87, s84, s35
	s_and_b64 s[40:41], s[40:41], exec
	s_cselect_b32 s41, s31, s87
	s_cselect_b32 s40, s30, s86
	s_add_u32 s100, s16, s34
	s_addc_u32 s101, s17, s35
	s_add_i32 m0, s59, 0xc000
	ds_read_b128 v[186:189], v207
	ds_read_b128 v[216:219], v207 offset:2048
	ds_read_b128 v[190:193], v208
	ds_read_b128 v[220:223], v208 offset:2048
	ds_read_b128 v[224:227], v207 offset:4096
	ds_read_b128 v[232:235], v207 offset:6144
	ds_read_b128 v[228:231], v208 offset:4096
	ds_read_b128 v[236:239], v208 offset:6144
	global_load_lds_dwordx4 v166, s[100:101]
	s_add_i32 m0, s59, 0xe000
	s_nop 0
	global_load_lds_dwordx4 v168, s[100:101]
	s_waitcnt vmcnt(8) lgkmcnt(0)
	s_setprio 1
	s_barrier
	s_cmp_eq_u32 s34, 0
	s_cbranch_scc1 .Lc0_P7_0
	v_mfma_f32_16x16x128_f8f6f4 v[156:159], v[24:31], v[186:193], v[156:159]
	v_mfma_f32_16x16x128_f8f6f4 v[152:155], v[16:23], v[186:193], v[152:155]
	v_mfma_f32_16x16x128_f8f6f4 v[136:139], v[16:23], v[216:223], v[136:139]
	v_mfma_f32_16x16x128_f8f6f4 v[140:143], v[24:31], v[216:223], v[140:143]
	v_mfma_f32_16x16x128_f8f6f4 v[124:127], v[24:31], v[224:231], v[124:127]
	v_mfma_f32_16x16x128_f8f6f4 v[120:123], v[16:23], v[224:231], v[120:123]
	v_mfma_f32_16x16x128_f8f6f4 v[104:107], v[16:23], v[232:239], v[104:107]
	v_mfma_f32_16x16x128_f8f6f4 v[108:111], v[24:31], v[232:239], v[108:111]
	v_mfma_f32_16x16x128_f8f6f4 v[148:151], v[8:15], v[186:193], v[148:151]
	v_mfma_f32_16x16x128_f8f6f4 v[144:147], v[0:7], v[186:193], v[144:147]
	v_mfma_f32_16x16x128_f8f6f4 v[128:131], v[0:7], v[216:223], v[128:131]
	v_mfma_f32_16x16x128_f8f6f4 v[132:135], v[8:15], v[216:223], v[132:135]
	v_mfma_f32_16x16x128_f8f6f4 v[116:119], v[8:15], v[224:231], v[116:119]
	v_mfma_f32_16x16x128_f8f6f4 v[112:115], v[0:7], v[224:231], v[112:115]
	v_mfma_f32_16x16x128_f8f6f4 v[96:99], v[0:7], v[232:239], v[96:99]
	v_mfma_f32_16x16x128_f8f6f4 v[100:103], v[8:15], v[232:239], v[100:103]
.Lc0b_P7_0:
	s_setprio 0
	s_barrier
	s_add_i32 s86, s69, s42
	s_mov_b32 m0, s86
	ds_read_b128 v[216:219], v207 offset:16384
	ds_read_b128 v[224:227], v207 offset:18432
	ds_read_b128 v[220:223], v208 offset:16384
	ds_read_b128 v[228:231], v208 offset:18432
	ds_read_b128 v[232:235], v207 offset:20480
	ds_read_b128 v[240:243], v207 offset:22528
	ds_read_b128 v[236:239], v208 offset:20480
	ds_read_b128 v[244:247], v208 offset:22528
	global_load_lds_dwordx4 v160, s[38:39]
	s_add_i32 m0, s86, 0x2000
	s_add_i32 s98, s71, s42
	global_load_lds_dwordx4 v162, s[38:39]
	s_mov_b32 m0, s98
	s_nop 0
	global_load_lds_dwordx4 v160, s[40:41]
	s_add_i32 m0, s98, 0x2000
	v_mov_b32_e32 v173, v165
	global_load_lds_dwordx4 v162, s[40:41]
	s_waitcnt vmcnt(6) lgkmcnt(0)
	s_setprio 1
	s_barrier
	s_cmp_eq_u32 s34, 0
	s_cbranch_scc1 .Lc0_P7_1
	v_mfma_f32_16x16x128_f8f6f4 v[92:95], v[24:31], v[216:223], v[92:95]
	v_mfma_f32_16x16x128_f8f6f4 v[88:91], v[16:23], v[216:223], v[88:91]
	v_mfma_f32_16x16x128_f8f6f4 v[72:75], v[16:23], v[224:231], v[72:75]
	v_mfma_f32_16x16x128_f8f6f4 v[76:79], v[24:31], v[224:231], v[76:79]
	s_mov_b32 m0, s59
	v_mfma_f32_16x16x128_f8f6f4 v[60:63], v[24:31], v[232:239], v[60:63]
	global_load_lds_dwordx4 v164, s[36:37]
	v_mfma_f32_16x16x128_f8f6f4 v[56:59], v[16:23], v[232:239], v[56:59]
	v_mfma_f32_16x16x128_f8f6f4 v[40:43], v[16:23], v[240:247], v[40:43]
	v_mfma_f32_16x16x128_f8f6f4 v[44:47], v[24:31], v[240:247], v[44:47]
	v_mfma_f32_16x16x128_f8f6f4 v[84:87], v[8:15], v[216:223], v[84:87]
	s_mov_b32 m0, s60
	v_mfma_f32_16x16x128_f8f6f4 v[80:83], v[0:7], v[216:223], v[80:83]
	global_load_lds_dwordx4 v172, s[36:37]
	v_mfma_f32_16x16x128_f8f6f4 v[64:67], v[0:7], v[224:231], v[64:67]
	v_mfma_f32_16x16x128_f8f6f4 v[68:71], v[8:15], v[224:231], v[68:71]
	v_mfma_f32_16x16x128_f8f6f4 v[52:55], v[8:15], v[232:239], v[52:55]
	v_mfma_f32_16x16x128_f8f6f4 v[48:51], v[0:7], v[232:239], v[48:51]
	v_mfma_f32_16x16x128_f8f6f4 v[32:35], v[0:7], v[240:247], v[32:35]
	v_mfma_f32_16x16x128_f8f6f4 v[36:39], v[8:15], v[240:247], v[36:39]
.Lc0b_P7_1:
	s_setprio 0
	s_barrier
	ds_read_b128 v[0:3], v252 offset:32768
	ds_read_b128 v[4:7], v253 offset:32768
	ds_read_b128 v[8:11], v252 offset:34816
	ds_read_b128 v[12:15], v253 offset:34816
	ds_read_b128 v[16:19], v252 offset:49152
	ds_read_b128 v[20:23], v253 offset:49152
	ds_read_b128 v[24:27], v252 offset:51200
	ds_read_b128 v[28:31], v253 offset:51200
	s_mov_b32 m0, s61
	ds_read_b128 v[216:219], v207 offset:32768
	ds_read_b128 v[224:227], v207 offset:34816
	ds_read_b128 v[220:223], v208 offset:32768
	ds_read_b128 v[228:231], v208 offset:34816
	ds_read_b128 v[232:235], v207 offset:36864
	ds_read_b128 v[240:243], v207 offset:38912
	ds_read_b128 v[236:239], v208 offset:36864
	ds_read_b128 v[244:247], v208 offset:38912
	global_load_lds_dwordx4 v184, s[36:37]
	s_mov_b32 m0, s62
	s_nop 0
	global_load_lds_dwordx4 v182, s[36:37]
	s_waitcnt vmcnt(8) lgkmcnt(0)
	s_setprio 1
	s_barrier
	v_mfma_f32_16x16x128_f8f6f4 v[156:159], v[0:7], v[216:223], v[156:159]
	v_mfma_f32_16x16x128_f8f6f4 v[152:155], v[8:15], v[216:223], v[152:155]
	v_mfma_f32_16x16x128_f8f6f4 v[136:139], v[8:15], v[224:231], v[136:139]
	v_mfma_f32_16x16x128_f8f6f4 v[140:143], v[0:7], v[224:231], v[140:143]
	v_mfma_f32_16x16x128_f8f6f4 v[124:127], v[0:7], v[232:239], v[124:127]
	v_mfma_f32_16x16x128_f8f6f4 v[120:123], v[8:15], v[232:239], v[120:123]
	v_mfma_f32_16x16x128_f8f6f4 v[104:107], v[8:15], v[240:247], v[104:107]
	v_mfma_f32_16x16x128_f8f6f4 v[108:111], v[0:7], v[240:247], v[108:111]
	v_mfma_f32_16x16x128_f8f6f4 v[148:151], v[16:23], v[216:223], v[148:151]
	v_mfma_f32_16x16x128_f8f6f4 v[144:147], v[24:31], v[216:223], v[144:147]
	v_mfma_f32_16x16x128_f8f6f4 v[128:131], v[24:31], v[224:231], v[128:131]
	v_mfma_f32_16x16x128_f8f6f4 v[132:135], v[16:23], v[224:231], v[132:135]
	v_mfma_f32_16x16x128_f8f6f4 v[116:119], v[16:23], v[232:239], v[116:119]
	v_mfma_f32_16x16x128_f8f6f4 v[112:115], v[24:31], v[232:239], v[112:115]
	v_mfma_f32_16x16x128_f8f6f4 v[96:99], v[24:31], v[240:247], v[96:99]
	v_mfma_f32_16x16x128_f8f6f4 v[100:103], v[16:23], v[240:247], v[100:103]
	s_setprio 0
	s_barrier
	s_add_i32 s99, s42, 0x17f80
	s_mov_b32 m0, s99
	ds_read_b128 v[216:219], v207 offset:49152
	ds_read_b128 v[224:227], v207 offset:51200
	ds_read_b128 v[220:223], v208 offset:49152
	ds_read_b128 v[228:231], v208 offset:51200
	ds_read_b128 v[232:235], v207 offset:53248
	ds_read_b128 v[240:243], v207 offset:55296
	ds_read_b128 v[236:239], v208 offset:53248
	ds_read_b128 v[244:247], v208 offset:55296
	global_load_lds_dwordx4 v160, s[38:39] offset:128
	s_add_i32 m0, s99, 0x2000
	s_add_i32 s99, s42, 0x1bf80
	global_load_lds_dwordx4 v162, s[38:39] offset:128
	s_mov_b32 m0, s99
	s_nop 0
	global_load_lds_dwordx4 v160, s[40:41] offset:128
	s_add_i32 m0, s99, 0x2000
	s_nop 0
	global_load_lds_dwordx4 v162, s[40:41] offset:128
	s_waitcnt vmcnt(6) lgkmcnt(0)
	s_setprio 1
	s_barrier
	v_mfma_f32_16x16x128_f8f6f4 v[92:95], v[0:7], v[216:223], v[92:95]
	v_mfma_f32_16x16x128_f8f6f4 v[88:91], v[8:15], v[216:223], v[88:91]
	v_mfma_f32_16x16x128_f8f6f4 v[72:75], v[8:15], v[224:231], v[72:75]
	v_mfma_f32_16x16x128_f8f6f4 v[76:79], v[0:7], v[224:231], v[76:79]
	s_add_i32 m0, s63, 0xffffff80
	v_mfma_f32_16x16x128_f8f6f4 v[60:63], v[0:7], v[232:239], v[60:63]
	global_load_lds_dwordx4 v164, s[36:37] offset:128
	v_mfma_f32_16x16x128_f8f6f4 v[56:59], v[8:15], v[232:239], v[56:59]
	v_mfma_f32_16x16x128_f8f6f4 v[40:43], v[8:15], v[240:247], v[40:43]
	v_mfma_f32_16x16x128_f8f6f4 v[44:47], v[0:7], v[240:247], v[44:47]
	v_mfma_f32_16x16x128_f8f6f4 v[84:87], v[16:23], v[216:223], v[84:87]
	s_add_i32 m0, s64, 0xffffff80
	v_mfma_f32_16x16x128_f8f6f4 v[80:83], v[24:31], v[216:223], v[80:83]
	global_load_lds_dwordx4 v172, s[36:37] offset:128
	v_mfma_f32_16x16x128_f8f6f4 v[64:67], v[24:31], v[224:231], v[64:67]
	v_mfma_f32_16x16x128_f8f6f4 v[68:71], v[16:23], v[224:231], v[68:71]
	v_mfma_f32_16x16x128_f8f6f4 v[52:55], v[16:23], v[232:239], v[52:55]
	v_mfma_f32_16x16x128_f8f6f4 v[48:51], v[24:31], v[232:239], v[48:51]
	v_mfma_f32_16x16x128_f8f6f4 v[32:35], v[24:31], v[240:247], v[32:35]
	v_mfma_f32_16x16x128_f8f6f4 v[36:39], v[16:23], v[240:247], v[36:39]
	s_setprio 0
	s_barrier
	s_add_i32 s85, s85, 2
	s_add_u32 s34, s34, 0x100
	s_addc_u32 s35, s35, 0
	s_cmp_gt_u32 s85, 5
	s_cbranch_scc1 .LBB0_675

.LBB0_817:
	s_add_u32 s28, s10, s26
	s_addc_u32 s29, s11, s27
	s_add_u32 s30, s28, 0x38000100
	s_addc_u32 s31, s29, 0
	ds_read_b128 v[24:27], v252
	ds_read_b128 v[28:31], v253
	s_and_b64 s[28:29], s[34:35], exec
	ds_read_b128 v[16:19], v252 offset:2048
	ds_read_b128 v[20:23], v253 offset:2048
	s_cselect_b32 s29, s1, s31
	s_cselect_b32 s28, s0, s30
	s_add_u32 s61, s56, s26
	ds_read_b128 v[8:11], v252 offset:16384
	ds_read_b128 v[12:15], v253 offset:16384
	s_addc_u32 s62, s57, s27
	ds_read_b128 v[0:3], v252 offset:18432
	ds_read_b128 v[4:7], v253 offset:18432
	s_and_b64 s[30:31], s[34:35], exec
	s_cselect_b32 s31, s23, s62
	s_cselect_b32 s30, s22, s61
	s_add_u32 s61, s58, s26
	s_addc_u32 s62, s59, s27
	s_and_b64 s[34:35], s[34:35], exec
	s_cselect_b32 s35, s25, s62
	s_cselect_b32 s34, s24, s61
	s_add_u32 s100, s14, s26
	s_addc_u32 s101, s15, s27
	s_add_i32 m0, s37, 0xc000
	ds_read_b128 v[186:189], v207
	ds_read_b128 v[216:219], v207 offset:2048
	ds_read_b128 v[190:193], v208
	ds_read_b128 v[220:223], v208 offset:2048
	ds_read_b128 v[224:227], v207 offset:4096
	ds_read_b128 v[232:235], v207 offset:6144
	ds_read_b128 v[228:231], v208 offset:4096
	ds_read_b128 v[236:239], v208 offset:6144
	global_load_lds_dwordx4 v168, s[100:101]
	s_add_i32 m0, s37, 0xe000
	s_nop 0
	global_load_lds_dwordx4 v170, s[100:101]
	s_waitcnt vmcnt(8) lgkmcnt(0)
	s_setprio 1
	s_barrier
	s_cmp_eq_u32 s26, 0
	s_cbranch_scc1 .Lc0_P9a_0
	v_mfma_f32_16x16x128_f8f6f4 v[156:159], v[24:31], v[186:193], v[156:159]
	v_mfma_f32_16x16x128_f8f6f4 v[152:155], v[16:23], v[186:193], v[152:155]
	v_mfma_f32_16x16x128_f8f6f4 v[136:139], v[16:23], v[216:223], v[136:139]
	v_mfma_f32_16x16x128_f8f6f4 v[140:143], v[24:31], v[216:223], v[140:143]
	v_mfma_f32_16x16x128_f8f6f4 v[124:127], v[24:31], v[224:231], v[124:127]
	v_mfma_f32_16x16x128_f8f6f4 v[120:123], v[16:23], v[224:231], v[120:123]
	v_mfma_f32_16x16x128_f8f6f4 v[104:107], v[16:23], v[232:239], v[104:107]
	v_mfma_f32_16x16x128_f8f6f4 v[108:111], v[24:31], v[232:239], v[108:111]
	v_mfma_f32_16x16x128_f8f6f4 v[148:151], v[8:15], v[186:193], v[148:151]
	v_mfma_f32_16x16x128_f8f6f4 v[144:147], v[0:7], v[186:193], v[144:147]
	v_mfma_f32_16x16x128_f8f6f4 v[128:131], v[0:7], v[216:223], v[128:131]
	v_mfma_f32_16x16x128_f8f6f4 v[132:135], v[8:15], v[216:223], v[132:135]
	v_mfma_f32_16x16x128_f8f6f4 v[116:119], v[8:15], v[224:231], v[116:119]
	v_mfma_f32_16x16x128_f8f6f4 v[112:115], v[0:7], v[224:231], v[112:115]
	v_mfma_f32_16x16x128_f8f6f4 v[96:99], v[0:7], v[232:239], v[96:99]
	v_mfma_f32_16x16x128_f8f6f4 v[100:103], v[8:15], v[232:239], v[100:103]
.Lc0b_P9a_0:
	s_setprio 0
	s_barrier
	s_add_i32 s61, s44, s36
	s_mov_b32 m0, s61
	ds_read_b128 v[216:219], v207 offset:16384
	ds_read_b128 v[224:227], v207 offset:18432
	ds_read_b128 v[220:223], v208 offset:16384
	ds_read_b128 v[228:231], v208 offset:18432
	ds_read_b128 v[232:235], v207 offset:20480
	ds_read_b128 v[240:243], v207 offset:22528
	ds_read_b128 v[236:239], v208 offset:20480
	ds_read_b128 v[244:247], v208 offset:22528
	global_load_lds_dwordx4 v160, s[30:31]
	s_add_i32 m0, s61, 0x2000
	s_add_i32 s98, s46, s36
	global_load_lds_dwordx4 v162, s[30:31]
	s_mov_b32 m0, s98
	s_nop 0
	global_load_lds_dwordx4 v160, s[34:35]
	s_add_i32 m0, s98, 0x2000
	v_mov_b32_e32 v167, v165
	global_load_lds_dwordx4 v162, s[34:35]
	s_waitcnt vmcnt(6) lgkmcnt(0)
	s_setprio 1
	s_barrier
	s_cmp_eq_u32 s26, 0
	s_cbranch_scc1 .Lc0_P9a_1
	v_mfma_f32_16x16x128_f8f6f4 v[92:95], v[24:31], v[216:223], v[92:95]
	v_mfma_f32_16x16x128_f8f6f4 v[88:91], v[16:23], v[216:223], v[88:91]
	v_mfma_f32_16x16x128_f8f6f4 v[72:75], v[16:23], v[224:231], v[72:75]
	v_mfma_f32_16x16x128_f8f6f4 v[76:79], v[24:31], v[224:231], v[76:79]
	s_mov_b32 m0, s37
	v_mfma_f32_16x16x128_f8f6f4 v[60:63], v[24:31], v[232:239], v[60:63]
	global_load_lds_dwordx4 v164, s[28:29]
	v_mfma_f32_16x16x128_f8f6f4 v[56:59], v[16:23], v[232:239], v[56:59]
	v_mfma_f32_16x16x128_f8f6f4 v[40:43], v[16:23], v[240:247], v[40:43]
	v_mfma_f32_16x16x128_f8f6f4 v[44:47], v[24:31], v[240:247], v[44:47]
	v_mfma_f32_16x16x128_f8f6f4 v[84:87], v[8:15], v[216:223], v[84:87]
	s_mov_b32 m0, s38
	v_mfma_f32_16x16x128_f8f6f4 v[80:83], v[0:7], v[216:223], v[80:83]
	global_load_lds_dwordx4 v166, s[28:29]
	v_mfma_f32_16x16x128_f8f6f4 v[64:67], v[0:7], v[224:231], v[64:67]
	v_mfma_f32_16x16x128_f8f6f4 v[68:71], v[8:15], v[224:231], v[68:71]
	v_mfma_f32_16x16x128_f8f6f4 v[52:55], v[8:15], v[232:239], v[52:55]
	v_mfma_f32_16x16x128_f8f6f4 v[48:51], v[0:7], v[232:239], v[48:51]
	v_mfma_f32_16x16x128_f8f6f4 v[32:35], v[0:7], v[240:247], v[32:35]
	v_mfma_f32_16x16x128_f8f6f4 v[36:39], v[8:15], v[240:247], v[36:39]
.Lc0b_P9a_1:
	s_setprio 0
	s_barrier
	ds_read_b128 v[0:3], v252 offset:32768
	ds_read_b128 v[4:7], v253 offset:32768
	ds_read_b128 v[8:11], v252 offset:34816
	ds_read_b128 v[12:15], v253 offset:34816
	ds_read_b128 v[16:19], v252 offset:49152
	ds_read_b128 v[20:23], v253 offset:49152
	ds_read_b128 v[24:27], v252 offset:51200
	ds_read_b128 v[28:31], v253 offset:51200
	s_mov_b32 m0, s39
	ds_read_b128 v[216:219], v207 offset:32768
	ds_read_b128 v[224:227], v207 offset:34816
	ds_read_b128 v[220:223], v208 offset:32768
	ds_read_b128 v[228:231], v208 offset:34816
	ds_read_b128 v[232:235], v207 offset:36864
	ds_read_b128 v[240:243], v207 offset:38912
	ds_read_b128 v[236:239], v208 offset:36864
	ds_read_b128 v[244:247], v208 offset:38912
	global_load_lds_dwordx4 v184, s[28:29]
	s_mov_b32 m0, s40
	s_nop 0
	global_load_lds_dwordx4 v182, s[28:29]
	s_waitcnt vmcnt(8) lgkmcnt(0)
	s_setprio 1
	s_barrier
	v_mfma_f32_16x16x128_f8f6f4 v[156:159], v[0:7], v[216:223], v[156:159]
	v_mfma_f32_16x16x128_f8f6f4 v[152:155], v[8:15], v[216:223], v[152:155]
	v_mfma_f32_16x16x128_f8f6f4 v[136:139], v[8:15], v[224:231], v[136:139]
	v_mfma_f32_16x16x128_f8f6f4 v[140:143], v[0:7], v[224:231], v[140:143]
	v_mfma_f32_16x16x128_f8f6f4 v[124:127], v[0:7], v[232:239], v[124:127]
	v_mfma_f32_16x16x128_f8f6f4 v[120:123], v[8:15], v[232:239], v[120:123]
	v_mfma_f32_16x16x128_f8f6f4 v[104:107], v[8:15], v[240:247], v[104:107]
	v_mfma_f32_16x16x128_f8f6f4 v[108:111], v[0:7], v[240:247], v[108:111]
	v_mfma_f32_16x16x128_f8f6f4 v[148:151], v[16:23], v[216:223], v[148:151]
	v_mfma_f32_16x16x128_f8f6f4 v[144:147], v[24:31], v[216:223], v[144:147]
	v_mfma_f32_16x16x128_f8f6f4 v[128:131], v[24:31], v[224:231], v[128:131]
	v_mfma_f32_16x16x128_f8f6f4 v[132:135], v[16:23], v[224:231], v[132:135]
	v_mfma_f32_16x16x128_f8f6f4 v[116:119], v[16:23], v[232:239], v[116:119]
	v_mfma_f32_16x16x128_f8f6f4 v[112:115], v[24:31], v[232:239], v[112:115]
	v_mfma_f32_16x16x128_f8f6f4 v[96:99], v[24:31], v[240:247], v[96:99]
	v_mfma_f32_16x16x128_f8f6f4 v[100:103], v[16:23], v[240:247], v[100:103]
	s_setprio 0
	s_barrier
	s_add_i32 s99, s36, 0x17f80
	s_mov_b32 m0, s99
	ds_read_b128 v[216:219], v207 offset:49152
	ds_read_b128 v[224:227], v207 offset:51200
	ds_read_b128 v[220:223], v208 offset:49152
	ds_read_b128 v[228:231], v208 offset:51200
	ds_read_b128 v[232:235], v207 offset:53248
	ds_read_b128 v[240:243], v207 offset:55296
	ds_read_b128 v[236:239], v208 offset:53248
	ds_read_b128 v[244:247], v208 offset:55296
	global_load_lds_dwordx4 v160, s[30:31] offset:128
	s_add_i32 m0, s99, 0x2000
	s_add_i32 s99, s36, 0x1bf80
	global_load_lds_dwordx4 v162, s[30:31] offset:128
	s_mov_b32 m0, s99
	s_nop 0
	global_load_lds_dwordx4 v160, s[34:35] offset:128
	s_add_i32 m0, s99, 0x2000
	s_nop 0
	global_load_lds_dwordx4 v162, s[34:35] offset:128
	s_waitcnt vmcnt(6) lgkmcnt(0)
	s_setprio 1
	s_barrier
	v_mfma_f32_16x16x128_f8f6f4 v[92:95], v[0:7], v[216:223], v[92:95]
	v_mfma_f32_16x16x128_f8f6f4 v[88:91], v[8:15], v[216:223], v[88:91]
	v_mfma_f32_16x16x128_f8f6f4 v[72:75], v[8:15], v[224:231], v[72:75]
	v_mfma_f32_16x16x128_f8f6f4 v[76:79], v[0:7], v[224:231], v[76:79]
	s_add_i32 m0, s41, 0xffffff80
	v_mfma_f32_16x16x128_f8f6f4 v[60:63], v[0:7], v[232:239], v[60:63]
	global_load_lds_dwordx4 v164, s[28:29] offset:128
	v_mfma_f32_16x16x128_f8f6f4 v[56:59], v[8:15], v[232:239], v[56:59]
	v_mfma_f32_16x16x128_f8f6f4 v[40:43], v[8:15], v[240:247], v[40:43]
	v_mfma_f32_16x16x128_f8f6f4 v[44:47], v[0:7], v[240:247], v[44:47]
	v_mfma_f32_16x16x128_f8f6f4 v[84:87], v[16:23], v[216:223], v[84:87]
	s_add_i32 m0, s42, 0xffffff80
	v_mfma_f32_16x16x128_f8f6f4 v[80:83], v[24:31], v[216:223], v[80:83]
	global_load_lds_dwordx4 v166, s[28:29] offset:128
	v_mfma_f32_16x16x128_f8f6f4 v[64:67], v[24:31], v[224:231], v[64:67]
	v_mfma_f32_16x16x128_f8f6f4 v[68:71], v[16:23], v[224:231], v[68:71]
	v_mfma_f32_16x16x128_f8f6f4 v[52:55], v[16:23], v[232:239], v[52:55]
	v_mfma_f32_16x16x128_f8f6f4 v[48:51], v[24:31], v[232:239], v[48:51]
	v_mfma_f32_16x16x128_f8f6f4 v[32:35], v[24:31], v[240:247], v[32:35]
	v_mfma_f32_16x16x128_f8f6f4 v[36:39], v[16:23], v[240:247], v[36:39]
	s_setprio 0
	s_barrier
	s_add_i32 s60, s60, 2
	s_add_u32 s26, s26, 0x100
	s_addc_u32 s27, s27, 0
	s_cmp_gt_u32 s60, 5
	s_cbranch_scc1 .LBB0_820

.LBB0_839:
	s_add_u32 s6, s10, s4
	s_addc_u32 s7, s11, s5
	s_add_u32 s34, s6, 0xe000100
	s_addc_u32 s35, s7, 0
	ds_read_b128 v[166:169], v252
	ds_read_b128 v[170:173], v253
	s_and_b64 s[6:7], s[30:31], exec
	ds_read_b128 v[174:177], v252 offset:2048
	ds_read_b128 v[178:181], v253 offset:2048
	s_cselect_b32 s7, s1, s35
	s_cselect_b32 s6, s0, s34
	s_add_u32 s62, s36, s4
	ds_read_b128 v[182:185], v252 offset:16384
	ds_read_b128 v[186:189], v253 offset:16384
	s_addc_u32 s63, s37, s5
	ds_read_b128 v[190:193], v252 offset:18432
	ds_read_b128 v[194:197], v253 offset:18432
	s_and_b64 s[34:35], s[30:31], exec
	s_cselect_b32 s35, s27, s63
	s_cselect_b32 s34, s26, s62
	s_add_u32 s62, s57, s4
	s_addc_u32 s63, s60, s5
	s_and_b64 s[30:31], s[30:31], exec
	s_cselect_b32 s31, s29, s63
	s_cselect_b32 s30, s28, s62
	v_lshl_add_u64 v[232:233], v[148:149], 0, s[4:5]
	s_add_i32 m0, s40, 0xc000
	ds_read_b128 v[200:203], v161
	ds_read_b128 v[204:207], v161 offset:1024
	ds_read_b128 v[208:211], v161 offset:2048
	ds_read_b128 v[212:215], v161 offset:3072
	ds_read_b128 v[216:219], v161 offset:4096
	ds_read_b128 v[220:223], v161 offset:5120
	ds_read_b128 v[224:227], v161 offset:6144
	ds_read_b128 v[228:231], v161 offset:7168
	global_load_lds_dwordx4 v[232:233], off
	v_lshl_add_u64 v[232:233], v[146:147], 0, s[4:5]
	s_add_i32 m0, s40, 0xe000
	s_nop 0
	global_load_lds_dwordx4 v[232:233], off
	s_waitcnt vmcnt(8) lgkmcnt(0)
	s_setprio 1
	s_barrier
	v_mfma_f32_16x16x32_bf16 v[124:127], v[166:169], v[200:203], v[124:127]
	v_mfma_f32_16x16x32_bf16 v[120:123], v[174:177], v[200:203], v[120:123]
	v_mfma_f32_16x16x32_bf16 v[108:111], v[166:169], v[208:211], v[108:111]
	v_mfma_f32_16x16x32_bf16 v[104:107], v[174:177], v[208:211], v[104:107]
	v_mfma_f32_16x16x32_bf16 v[92:95], v[166:169], v[216:219], v[92:95]
	v_mfma_f32_16x16x32_bf16 v[88:91], v[174:177], v[216:219], v[88:91]
	v_mfma_f32_16x16x32_bf16 v[76:79], v[166:169], v[224:227], v[76:79]
	v_mfma_f32_16x16x32_bf16 v[72:75], v[174:177], v[224:227], v[72:75]
	v_mfma_f32_16x16x32_bf16 v[124:127], v[170:173], v[204:207], v[124:127]
	v_mfma_f32_16x16x32_bf16 v[120:123], v[178:181], v[204:207], v[120:123]
	v_mfma_f32_16x16x32_bf16 v[108:111], v[170:173], v[212:215], v[108:111]
	v_mfma_f32_16x16x32_bf16 v[104:107], v[178:181], v[212:215], v[104:107]
	v_mfma_f32_16x16x32_bf16 v[92:95], v[170:173], v[220:223], v[92:95]
	v_mfma_f32_16x16x32_bf16 v[88:91], v[178:181], v[220:223], v[88:91]
	v_mfma_f32_16x16x32_bf16 v[76:79], v[170:173], v[228:231], v[76:79]
	v_mfma_f32_16x16x32_bf16 v[72:75], v[178:181], v[228:231], v[72:75]
	v_mfma_f32_16x16x32_bf16 v[116:119], v[182:185], v[200:203], v[116:119]
	v_mfma_f32_16x16x32_bf16 v[112:115], v[190:193], v[200:203], v[112:115]
	v_mfma_f32_16x16x32_bf16 v[100:103], v[182:185], v[208:211], v[100:103]
	v_mfma_f32_16x16x32_bf16 v[96:99], v[190:193], v[208:211], v[96:99]
	v_mfma_f32_16x16x32_bf16 v[84:87], v[182:185], v[216:219], v[84:87]
	v_mfma_f32_16x16x32_bf16 v[80:83], v[190:193], v[216:219], v[80:83]
	v_mfma_f32_16x16x32_bf16 v[68:71], v[182:185], v[224:227], v[68:71]
	v_mfma_f32_16x16x32_bf16 v[64:67], v[190:193], v[224:227], v[64:67]
	v_mfma_f32_16x16x32_bf16 v[116:119], v[186:189], v[204:207], v[116:119]
	v_mfma_f32_16x16x32_bf16 v[112:115], v[194:197], v[204:207], v[112:115]
	v_mfma_f32_16x16x32_bf16 v[100:103], v[186:189], v[212:215], v[100:103]
	v_mfma_f32_16x16x32_bf16 v[96:99], v[194:197], v[212:215], v[96:99]
	v_mfma_f32_16x16x32_bf16 v[84:87], v[186:189], v[220:223], v[84:87]
	v_mfma_f32_16x16x32_bf16 v[80:83], v[194:197], v[220:223], v[80:83]
	v_mfma_f32_16x16x32_bf16 v[68:71], v[186:189], v[228:231], v[68:71]
	v_mfma_f32_16x16x32_bf16 v[64:67], v[194:197], v[228:231], v[64:67]
	s_setprio 0
	s_barrier
	s_add_i32 s62, s49, s39
	v_lshl_add_u64 v[232:233], s[34:35], 0, v[132:133]
	s_mov_b32 m0, s62
	ds_read_b128 v[200:203], v161 offset:16384
	ds_read_b128 v[204:207], v161 offset:17408
	ds_read_b128 v[208:211], v161 offset:18432
	ds_read_b128 v[212:215], v161 offset:19456
	ds_read_b128 v[216:219], v161 offset:20480
	ds_read_b128 v[220:223], v161 offset:21504
	ds_read_b128 v[224:227], v161 offset:22528
	ds_read_b128 v[228:231], v161 offset:23552
	global_load_lds_dwordx4 v[232:233], off
	v_lshl_add_u64 v[234:235], s[34:35], 0, v[134:135]
	s_add_i32 m0, s62, 0x2000
	s_add_i32 s34, s51, s39
	global_load_lds_dwordx4 v[234:235], off
	v_lshl_add_u64 v[236:237], s[30:31], 0, v[132:133]
	s_mov_b32 m0, s34
	v_lshl_add_u64 v[238:239], s[30:31], 0, v[134:135]
	global_load_lds_dwordx4 v[236:237], off
	s_add_i32 m0, s34, 0x2000
	v_mov_b32_e32 v139, v137
	global_load_lds_dwordx4 v[238:239], off
	s_mov_b32 m0, s40
	v_lshl_add_u64 v[240:241], s[6:7], 0, v[136:137]
	global_load_lds_dwordx4 v136, s[6:7]
	s_mov_b32 m0, s41
	v_lshl_add_u64 v[242:243], s[6:7], 0, v[138:139]
	global_load_lds_dwordx4 v138, s[6:7]
	s_waitcnt vmcnt(8) lgkmcnt(0)
	s_setprio 1
	s_barrier
	v_mfma_f32_16x16x32_bf16 v[60:63], v[166:169], v[200:203], v[60:63]
	v_mfma_f32_16x16x32_bf16 v[56:59], v[174:177], v[200:203], v[56:59]
	v_mfma_f32_16x16x32_bf16 v[44:47], v[166:169], v[208:211], v[44:47]
	v_mfma_f32_16x16x32_bf16 v[40:43], v[174:177], v[208:211], v[40:43]
	v_mfma_f32_16x16x32_bf16 v[28:31], v[166:169], v[216:219], v[28:31]
	v_mfma_f32_16x16x32_bf16 v[24:27], v[174:177], v[216:219], v[24:27]
	v_mfma_f32_16x16x32_bf16 v[12:15], v[166:169], v[224:227], v[12:15]
	v_mfma_f32_16x16x32_bf16 v[8:11], v[174:177], v[224:227], v[8:11]
	v_mfma_f32_16x16x32_bf16 v[60:63], v[170:173], v[204:207], v[60:63]
	v_mfma_f32_16x16x32_bf16 v[56:59], v[178:181], v[204:207], v[56:59]
	v_mfma_f32_16x16x32_bf16 v[44:47], v[170:173], v[212:215], v[44:47]
	v_mfma_f32_16x16x32_bf16 v[40:43], v[178:181], v[212:215], v[40:43]
	v_mfma_f32_16x16x32_bf16 v[28:31], v[170:173], v[220:223], v[28:31]
	v_mfma_f32_16x16x32_bf16 v[24:27], v[178:181], v[220:223], v[24:27]
	v_mfma_f32_16x16x32_bf16 v[12:15], v[170:173], v[228:231], v[12:15]
	v_mfma_f32_16x16x32_bf16 v[8:11], v[178:181], v[228:231], v[8:11]
	v_mfma_f32_16x16x32_bf16 v[52:55], v[182:185], v[200:203], v[52:55]
	v_mfma_f32_16x16x32_bf16 v[48:51], v[190:193], v[200:203], v[48:51]
	v_mfma_f32_16x16x32_bf16 v[36:39], v[182:185], v[208:211], v[36:39]
	v_mfma_f32_16x16x32_bf16 v[32:35], v[190:193], v[208:211], v[32:35]
	v_mfma_f32_16x16x32_bf16 v[20:23], v[182:185], v[216:219], v[20:23]
	v_mfma_f32_16x16x32_bf16 v[16:19], v[190:193], v[216:219], v[16:19]
	v_mfma_f32_16x16x32_bf16 v[4:7], v[182:185], v[224:227], v[4:7]
	v_mfma_f32_16x16x32_bf16 v[0:3], v[190:193], v[224:227], v[0:3]
	v_mfma_f32_16x16x32_bf16 v[52:55], v[186:189], v[204:207], v[52:55]
	v_mfma_f32_16x16x32_bf16 v[48:51], v[194:197], v[204:207], v[48:51]
	v_mfma_f32_16x16x32_bf16 v[36:39], v[186:189], v[212:215], v[36:39]
	v_mfma_f32_16x16x32_bf16 v[32:35], v[194:197], v[212:215], v[32:35]
	v_mfma_f32_16x16x32_bf16 v[20:23], v[186:189], v[220:223], v[20:23]
	v_mfma_f32_16x16x32_bf16 v[16:19], v[194:197], v[220:223], v[16:19]
	v_mfma_f32_16x16x32_bf16 v[4:7], v[186:189], v[228:231], v[4:7]
	v_mfma_f32_16x16x32_bf16 v[0:3], v[194:197], v[228:231], v[0:3]
	s_setprio 0
	s_barrier
	s_add_i32 s30, 0, 0x18000
	ds_read_b128 v[166:169], v252 offset:32768
	ds_read_b128 v[170:173], v253 offset:32768
	s_add_i32 s31, 0, 0x1c000
	ds_read_b128 v[174:177], v252 offset:34816
	ds_read_b128 v[178:181], v253 offset:34816
	ds_read_b128 v[182:185], v252 offset:49152
	ds_read_b128 v[186:189], v253 offset:49152
	ds_read_b128 v[190:193], v252 offset:51200
	ds_read_b128 v[194:197], v253 offset:51200
	s_mov_b32 m0, s42
	v_lshl_add_u64 v[152:153], s[6:7], 0, v[152:153]
	ds_read_b128 v[200:203], v161 offset:32768
	ds_read_b128 v[204:207], v161 offset:33792
	ds_read_b128 v[208:211], v161 offset:34816
	ds_read_b128 v[212:215], v161 offset:35840
	ds_read_b128 v[216:219], v161 offset:36864
	ds_read_b128 v[220:223], v161 offset:37888
	ds_read_b128 v[224:227], v161 offset:38912
	ds_read_b128 v[228:231], v161 offset:39936
	global_load_lds_dwordx4 v[152:153], off
	v_lshl_add_u64 v[150:151], s[6:7], 0, v[150:151]
	s_mov_b32 m0, s43
	s_nop 0
	global_load_lds_dwordx4 v[150:151], off
	s_waitcnt vmcnt(8) lgkmcnt(0)
	s_setprio 1
	s_barrier
	v_mfma_f32_16x16x32_bf16 v[124:127], v[166:169], v[200:203], v[124:127]
	v_mfma_f32_16x16x32_bf16 v[120:123], v[174:177], v[200:203], v[120:123]
	v_mfma_f32_16x16x32_bf16 v[108:111], v[166:169], v[208:211], v[108:111]
	v_mfma_f32_16x16x32_bf16 v[104:107], v[174:177], v[208:211], v[104:107]
	v_mfma_f32_16x16x32_bf16 v[92:95], v[166:169], v[216:219], v[92:95]
	v_mfma_f32_16x16x32_bf16 v[88:91], v[174:177], v[216:219], v[88:91]
	v_mfma_f32_16x16x32_bf16 v[76:79], v[166:169], v[224:227], v[76:79]
	v_mfma_f32_16x16x32_bf16 v[72:75], v[174:177], v[224:227], v[72:75]
	v_mfma_f32_16x16x32_bf16 v[124:127], v[170:173], v[204:207], v[124:127]
	v_mfma_f32_16x16x32_bf16 v[120:123], v[178:181], v[204:207], v[120:123]
	v_mfma_f32_16x16x32_bf16 v[108:111], v[170:173], v[212:215], v[108:111]
	v_mfma_f32_16x16x32_bf16 v[104:107], v[178:181], v[212:215], v[104:107]
	v_mfma_f32_16x16x32_bf16 v[92:95], v[170:173], v[220:223], v[92:95]
	v_mfma_f32_16x16x32_bf16 v[88:91], v[178:181], v[220:223], v[88:91]
	v_mfma_f32_16x16x32_bf16 v[76:79], v[170:173], v[228:231], v[76:79]
	v_mfma_f32_16x16x32_bf16 v[72:75], v[178:181], v[228:231], v[72:75]
	v_mfma_f32_16x16x32_bf16 v[116:119], v[182:185], v[200:203], v[116:119]
	v_mfma_f32_16x16x32_bf16 v[112:115], v[190:193], v[200:203], v[112:115]
	v_mfma_f32_16x16x32_bf16 v[100:103], v[182:185], v[208:211], v[100:103]
	v_mfma_f32_16x16x32_bf16 v[96:99], v[190:193], v[208:211], v[96:99]
	v_mfma_f32_16x16x32_bf16 v[84:87], v[182:185], v[216:219], v[84:87]
	v_mfma_f32_16x16x32_bf16 v[80:83], v[190:193], v[216:219], v[80:83]
	v_mfma_f32_16x16x32_bf16 v[68:71], v[182:185], v[224:227], v[68:71]
	v_mfma_f32_16x16x32_bf16 v[64:67], v[190:193], v[224:227], v[64:67]
	v_mfma_f32_16x16x32_bf16 v[116:119], v[186:189], v[204:207], v[116:119]
	v_mfma_f32_16x16x32_bf16 v[112:115], v[194:197], v[204:207], v[112:115]
	v_mfma_f32_16x16x32_bf16 v[100:103], v[186:189], v[212:215], v[100:103]
	v_mfma_f32_16x16x32_bf16 v[96:99], v[194:197], v[212:215], v[96:99]
	v_mfma_f32_16x16x32_bf16 v[84:87], v[186:189], v[220:223], v[84:87]
	v_mfma_f32_16x16x32_bf16 v[80:83], v[194:197], v[220:223], v[80:83]
	v_mfma_f32_16x16x32_bf16 v[68:71], v[186:189], v[228:231], v[68:71]
	v_mfma_f32_16x16x32_bf16 v[64:67], v[194:197], v[228:231], v[64:67]
	s_setprio 0
	s_barrier
	s_add_i32 s6, s30, s39
	v_lshl_add_u64 v[228:229], v[232:233], 0, s[20:21]
	s_mov_b32 m0, s6
	ds_read_b128 v[150:153], v161 offset:49152
	ds_read_b128 v[200:203], v161 offset:50176
	ds_read_b128 v[204:207], v161 offset:51200
	ds_read_b128 v[208:211], v161 offset:52224
	ds_read_b128 v[212:215], v161 offset:53248
	ds_read_b128 v[216:219], v161 offset:54272
	ds_read_b128 v[220:223], v161 offset:55296
	ds_read_b128 v[224:227], v161 offset:56320
	global_load_lds_dwordx4 v[228:229], off
	v_lshl_add_u64 v[228:229], v[234:235], 0, s[20:21]
	s_add_i32 m0, s6, 0x2000
	s_add_i32 s6, s31, s39
	global_load_lds_dwordx4 v[228:229], off
	v_lshl_add_u64 v[228:229], v[236:237], 0, s[20:21]
	s_mov_b32 m0, s6
	s_nop 0
	global_load_lds_dwordx4 v[228:229], off
	v_lshl_add_u64 v[228:229], v[238:239], 0, s[20:21]
	s_add_i32 m0, s6, 0x2000
	s_nop 0
	global_load_lds_dwordx4 v[228:229], off
	v_lshl_add_u64 v[228:229], v[240:241], 0, s[20:21]
	s_mov_b32 m0, s47
	s_nop 0
	global_load_lds_dwordx4 v[228:229], off
	v_lshl_add_u64 v[228:229], v[242:243], 0, s[20:21]
	s_mov_b32 m0, s48
	s_nop 0
	global_load_lds_dwordx4 v[228:229], off
	s_waitcnt vmcnt(8) lgkmcnt(0)
	s_setprio 1
	s_barrier
	v_mfma_f32_16x16x32_bf16 v[60:63], v[166:169], v[150:153], v[60:63]
	v_mfma_f32_16x16x32_bf16 v[56:59], v[174:177], v[150:153], v[56:59]
	v_mfma_f32_16x16x32_bf16 v[44:47], v[166:169], v[204:207], v[44:47]
	v_mfma_f32_16x16x32_bf16 v[40:43], v[174:177], v[204:207], v[40:43]
	v_mfma_f32_16x16x32_bf16 v[28:31], v[166:169], v[212:215], v[28:31]
	v_mfma_f32_16x16x32_bf16 v[24:27], v[174:177], v[212:215], v[24:27]
	v_mfma_f32_16x16x32_bf16 v[12:15], v[166:169], v[220:223], v[12:15]
	v_mfma_f32_16x16x32_bf16 v[8:11], v[174:177], v[220:223], v[8:11]
	v_mfma_f32_16x16x32_bf16 v[60:63], v[170:173], v[200:203], v[60:63]
	v_mfma_f32_16x16x32_bf16 v[56:59], v[178:181], v[200:203], v[56:59]
	v_mfma_f32_16x16x32_bf16 v[44:47], v[170:173], v[208:211], v[44:47]
	v_mfma_f32_16x16x32_bf16 v[40:43], v[178:181], v[208:211], v[40:43]
	v_mfma_f32_16x16x32_bf16 v[28:31], v[170:173], v[216:219], v[28:31]
	v_mfma_f32_16x16x32_bf16 v[24:27], v[178:181], v[216:219], v[24:27]
	v_mfma_f32_16x16x32_bf16 v[12:15], v[170:173], v[224:227], v[12:15]
	v_mfma_f32_16x16x32_bf16 v[8:11], v[178:181], v[224:227], v[8:11]
	v_mfma_f32_16x16x32_bf16 v[52:55], v[182:185], v[150:153], v[52:55]
	v_mfma_f32_16x16x32_bf16 v[48:51], v[190:193], v[150:153], v[48:51]
	v_mfma_f32_16x16x32_bf16 v[36:39], v[182:185], v[204:207], v[36:39]
	v_mfma_f32_16x16x32_bf16 v[32:35], v[190:193], v[204:207], v[32:35]
	v_mfma_f32_16x16x32_bf16 v[20:23], v[182:185], v[212:215], v[20:23]
	v_mfma_f32_16x16x32_bf16 v[16:19], v[190:193], v[212:215], v[16:19]
	v_mfma_f32_16x16x32_bf16 v[4:7], v[182:185], v[220:223], v[4:7]
	v_mfma_f32_16x16x32_bf16 v[0:3], v[190:193], v[220:223], v[0:3]
	v_mfma_f32_16x16x32_bf16 v[52:55], v[186:189], v[200:203], v[52:55]
	v_mfma_f32_16x16x32_bf16 v[48:51], v[194:197], v[200:203], v[48:51]
	v_mfma_f32_16x16x32_bf16 v[36:39], v[186:189], v[208:211], v[36:39]
	v_mfma_f32_16x16x32_bf16 v[32:35], v[194:197], v[208:211], v[32:35]
	v_mfma_f32_16x16x32_bf16 v[20:23], v[186:189], v[216:219], v[20:23]
	v_mfma_f32_16x16x32_bf16 v[16:19], v[194:197], v[216:219], v[16:19]
	v_mfma_f32_16x16x32_bf16 v[4:7], v[186:189], v[224:227], v[4:7]
	v_mfma_f32_16x16x32_bf16 v[0:3], v[194:197], v[224:227], v[0:3]
	s_setprio 0
	s_barrier
	s_add_i32 s61, s61, 2
	s_add_u32 s4, s4, 0x100
	s_addc_u32 s5, s5, 0
	s_cmp_gt_u32 s61, 13
	s_cbranch_scc1 .LBB0_842

.LBB0_1549:
	s_add_u32 s26, s4, s24
	s_addc_u32 s27, s5, s25
	s_add_u32 s28, s26, 0x28000100
	s_addc_u32 s29, s27, 0
	ds_read_b128 v[24:27], v252
	ds_read_b128 v[28:31], v253
	s_and_b64 s[26:27], s[30:31], exec
	ds_read_b128 v[16:19], v252 offset:2048
	ds_read_b128 v[20:23], v253 offset:2048
	s_cselect_b32 s27, s7, s29
	s_cselect_b32 s26, s6, s28
	s_add_u32 s63, s58, s24
	ds_read_b128 v[8:11], v252 offset:16384
	ds_read_b128 v[12:15], v253 offset:16384
	s_addc_u32 s64, s59, s25
	ds_read_b128 v[0:3], v252 offset:18432
	ds_read_b128 v[4:7], v253 offset:18432
	s_and_b64 s[28:29], s[30:31], exec
	s_cselect_b32 s29, s21, s64
	s_cselect_b32 s28, s20, s63
	s_add_u32 s63, s60, s24
	s_addc_u32 s64, s61, s25
	s_and_b64 s[30:31], s[30:31], exec
	s_cselect_b32 s31, s23, s64
	s_cselect_b32 s30, s22, s63
	s_add_u32 s100, s14, s24
	s_addc_u32 s101, s15, s25
	s_add_i32 m0, s35, 0xc000
	ds_read_b128 v[186:189], v206
	ds_read_b128 v[214:217], v206 offset:2048
	ds_read_b128 v[190:193], v207
	ds_read_b128 v[218:221], v207 offset:2048
	ds_read_b128 v[222:225], v206 offset:4096
	ds_read_b128 v[230:233], v206 offset:6144
	ds_read_b128 v[226:229], v207 offset:4096
	ds_read_b128 v[234:237], v207 offset:6144
	global_load_lds_dwordx4 v168, s[100:101]
	s_add_i32 m0, s35, 0xe000
	s_nop 0
	global_load_lds_dwordx4 v170, s[100:101]
	s_waitcnt vmcnt(8) lgkmcnt(0)
	s_setprio 1
	s_barrier
	s_cmp_eq_u32 s24, 0
	s_cbranch_scc1 .Lc0_P12_0
	v_mfma_f32_16x16x128_f8f6f4 v[156:159], v[24:31], v[186:193], v[156:159]
	v_mfma_f32_16x16x128_f8f6f4 v[152:155], v[16:23], v[186:193], v[152:155]
	v_mfma_f32_16x16x128_f8f6f4 v[136:139], v[16:23], v[214:221], v[136:139]
	v_mfma_f32_16x16x128_f8f6f4 v[144:147], v[24:31], v[214:221], v[144:147]
	v_mfma_f32_16x16x128_f8f6f4 v[124:127], v[24:31], v[222:229], v[124:127]
	v_mfma_f32_16x16x128_f8f6f4 v[120:123], v[16:23], v[222:229], v[120:123]
	v_mfma_f32_16x16x128_f8f6f4 v[104:107], v[16:23], v[230:237], v[104:107]
	v_mfma_f32_16x16x128_f8f6f4 v[112:115], v[24:31], v[230:237], v[112:115]
	v_mfma_f32_16x16x128_f8f6f4 v[148:151], v[8:15], v[186:193], v[148:151]
	v_mfma_f32_16x16x128_f8f6f4 v[140:143], v[0:7], v[186:193], v[140:143]
	v_mfma_f32_16x16x128_f8f6f4 v[128:131], v[0:7], v[214:221], v[128:131]
	v_mfma_f32_16x16x128_f8f6f4 v[132:135], v[8:15], v[214:221], v[132:135]
	v_mfma_f32_16x16x128_f8f6f4 v[116:119], v[8:15], v[222:229], v[116:119]
	v_mfma_f32_16x16x128_f8f6f4 v[108:111], v[0:7], v[222:229], v[108:111]
	v_mfma_f32_16x16x128_f8f6f4 v[96:99], v[0:7], v[230:237], v[96:99]
	v_mfma_f32_16x16x128_f8f6f4 v[100:103], v[8:15], v[230:237], v[100:103]
.Lc0b_P12_0:
	s_setprio 0
	s_barrier
	s_add_i32 s63, s46, s34
	s_mov_b32 m0, s63
	ds_read_b128 v[214:217], v206 offset:16384
	ds_read_b128 v[222:225], v206 offset:18432
	ds_read_b128 v[218:221], v207 offset:16384
	ds_read_b128 v[226:229], v207 offset:18432
	ds_read_b128 v[230:233], v206 offset:20480
	ds_read_b128 v[238:241], v206 offset:22528
	ds_read_b128 v[234:237], v207 offset:20480
	ds_read_b128 v[242:245], v207 offset:22528
	global_load_lds_dwordx4 v160, s[28:29]
	s_add_i32 m0, s63, 0x2000
	s_add_i32 s98, s48, s34
	global_load_lds_dwordx4 v162, s[28:29]
	s_mov_b32 m0, s98
	s_nop 0
	global_load_lds_dwordx4 v160, s[30:31]
	s_add_i32 m0, s98, 0x2000
	v_mov_b32_e32 v167, v165
	global_load_lds_dwordx4 v162, s[30:31]
	s_waitcnt vmcnt(6) lgkmcnt(0)
	s_setprio 1
	s_barrier
	s_cmp_eq_u32 s24, 0
	s_cbranch_scc1 .Lc0_P12_1
	v_mfma_f32_16x16x128_f8f6f4 v[92:95], v[24:31], v[214:221], v[92:95]
	v_mfma_f32_16x16x128_f8f6f4 v[88:91], v[16:23], v[214:221], v[88:91]
	v_mfma_f32_16x16x128_f8f6f4 v[72:75], v[16:23], v[222:229], v[72:75]
	v_mfma_f32_16x16x128_f8f6f4 v[80:83], v[24:31], v[222:229], v[80:83]
	s_mov_b32 m0, s35
	v_mfma_f32_16x16x128_f8f6f4 v[60:63], v[24:31], v[230:237], v[60:63]
	global_load_lds_dwordx4 v164, s[26:27]
	v_mfma_f32_16x16x128_f8f6f4 v[56:59], v[16:23], v[230:237], v[56:59]
	v_mfma_f32_16x16x128_f8f6f4 v[40:43], v[16:23], v[238:245], v[40:43]
	v_mfma_f32_16x16x128_f8f6f4 v[48:51], v[24:31], v[238:245], v[48:51]
	v_mfma_f32_16x16x128_f8f6f4 v[84:87], v[8:15], v[214:221], v[84:87]
	s_mov_b32 m0, s36
	v_mfma_f32_16x16x128_f8f6f4 v[76:79], v[0:7], v[214:221], v[76:79]
	global_load_lds_dwordx4 v166, s[26:27]
	v_mfma_f32_16x16x128_f8f6f4 v[64:67], v[0:7], v[222:229], v[64:67]
	v_mfma_f32_16x16x128_f8f6f4 v[68:71], v[8:15], v[222:229], v[68:71]
	v_mfma_f32_16x16x128_f8f6f4 v[52:55], v[8:15], v[230:237], v[52:55]
	v_mfma_f32_16x16x128_f8f6f4 v[44:47], v[0:7], v[230:237], v[44:47]
	v_mfma_f32_16x16x128_f8f6f4 v[32:35], v[0:7], v[238:245], v[32:35]
	v_mfma_f32_16x16x128_f8f6f4 v[36:39], v[8:15], v[238:245], v[36:39]
.Lc0b_P12_1:
	s_setprio 0
	s_barrier
	ds_read_b128 v[0:3], v252 offset:32768
	ds_read_b128 v[4:7], v253 offset:32768
	ds_read_b128 v[8:11], v252 offset:34816
	ds_read_b128 v[12:15], v253 offset:34816
	ds_read_b128 v[16:19], v252 offset:49152
	ds_read_b128 v[20:23], v253 offset:49152
	ds_read_b128 v[24:27], v252 offset:51200
	ds_read_b128 v[28:31], v253 offset:51200
	s_mov_b32 m0, s37
	ds_read_b128 v[214:217], v206 offset:32768
	ds_read_b128 v[222:225], v206 offset:34816
	ds_read_b128 v[218:221], v207 offset:32768
	ds_read_b128 v[226:229], v207 offset:34816
	ds_read_b128 v[230:233], v206 offset:36864
	ds_read_b128 v[238:241], v206 offset:38912
	ds_read_b128 v[234:237], v207 offset:36864
	ds_read_b128 v[242:245], v207 offset:38912
	global_load_lds_dwordx4 v184, s[26:27]
	s_mov_b32 m0, s38
	s_nop 0
	global_load_lds_dwordx4 v182, s[26:27]
	s_waitcnt vmcnt(8) lgkmcnt(0)
	s_setprio 1
	s_barrier
	v_mfma_f32_16x16x128_f8f6f4 v[156:159], v[0:7], v[214:221], v[156:159]
	v_mfma_f32_16x16x128_f8f6f4 v[152:155], v[8:15], v[214:221], v[152:155]
	v_mfma_f32_16x16x128_f8f6f4 v[136:139], v[8:15], v[222:229], v[136:139]
	v_mfma_f32_16x16x128_f8f6f4 v[144:147], v[0:7], v[222:229], v[144:147]
	v_mfma_f32_16x16x128_f8f6f4 v[124:127], v[0:7], v[230:237], v[124:127]
	v_mfma_f32_16x16x128_f8f6f4 v[120:123], v[8:15], v[230:237], v[120:123]
	v_mfma_f32_16x16x128_f8f6f4 v[104:107], v[8:15], v[238:245], v[104:107]
	v_mfma_f32_16x16x128_f8f6f4 v[112:115], v[0:7], v[238:245], v[112:115]
	v_mfma_f32_16x16x128_f8f6f4 v[148:151], v[16:23], v[214:221], v[148:151]
	v_mfma_f32_16x16x128_f8f6f4 v[140:143], v[24:31], v[214:221], v[140:143]
	v_mfma_f32_16x16x128_f8f6f4 v[128:131], v[24:31], v[222:229], v[128:131]
	v_mfma_f32_16x16x128_f8f6f4 v[132:135], v[16:23], v[222:229], v[132:135]
	v_mfma_f32_16x16x128_f8f6f4 v[116:119], v[16:23], v[230:237], v[116:119]
	v_mfma_f32_16x16x128_f8f6f4 v[108:111], v[24:31], v[230:237], v[108:111]
	v_mfma_f32_16x16x128_f8f6f4 v[96:99], v[24:31], v[238:245], v[96:99]
	v_mfma_f32_16x16x128_f8f6f4 v[100:103], v[16:23], v[238:245], v[100:103]
	s_setprio 0
	s_barrier
	s_add_i32 s99, s34, 0x17f80
	s_mov_b32 m0, s99
	ds_read_b128 v[214:217], v206 offset:49152
	ds_read_b128 v[222:225], v206 offset:51200
	ds_read_b128 v[218:221], v207 offset:49152
	ds_read_b128 v[226:229], v207 offset:51200
	ds_read_b128 v[230:233], v206 offset:53248
	ds_read_b128 v[238:241], v206 offset:55296
	ds_read_b128 v[234:237], v207 offset:53248
	ds_read_b128 v[242:245], v207 offset:55296
	global_load_lds_dwordx4 v160, s[28:29] offset:128
	s_add_i32 m0, s99, 0x2000
	s_add_i32 s99, s34, 0x1bf80
	global_load_lds_dwordx4 v162, s[28:29] offset:128
	s_mov_b32 m0, s99
	s_nop 0
	global_load_lds_dwordx4 v160, s[30:31] offset:128
	s_add_i32 m0, s99, 0x2000
	s_nop 0
	global_load_lds_dwordx4 v162, s[30:31] offset:128
	s_waitcnt vmcnt(6) lgkmcnt(0)
	s_setprio 1
	s_barrier
	v_mfma_f32_16x16x128_f8f6f4 v[92:95], v[0:7], v[214:221], v[92:95]
	v_mfma_f32_16x16x128_f8f6f4 v[88:91], v[8:15], v[214:221], v[88:91]
	v_mfma_f32_16x16x128_f8f6f4 v[72:75], v[8:15], v[222:229], v[72:75]
	v_mfma_f32_16x16x128_f8f6f4 v[80:83], v[0:7], v[222:229], v[80:83]
	s_add_i32 m0, s41, 0xffffff80
	v_mfma_f32_16x16x128_f8f6f4 v[60:63], v[0:7], v[230:237], v[60:63]
	global_load_lds_dwordx4 v164, s[26:27] offset:128
	v_mfma_f32_16x16x128_f8f6f4 v[56:59], v[8:15], v[230:237], v[56:59]
	v_mfma_f32_16x16x128_f8f6f4 v[40:43], v[8:15], v[238:245], v[40:43]
	v_mfma_f32_16x16x128_f8f6f4 v[48:51], v[0:7], v[238:245], v[48:51]
	v_mfma_f32_16x16x128_f8f6f4 v[84:87], v[16:23], v[214:221], v[84:87]
	s_add_i32 m0, s42, 0xffffff80
	v_mfma_f32_16x16x128_f8f6f4 v[76:79], v[24:31], v[214:221], v[76:79]
	global_load_lds_dwordx4 v166, s[26:27] offset:128
	v_mfma_f32_16x16x128_f8f6f4 v[64:67], v[24:31], v[222:229], v[64:67]
	v_mfma_f32_16x16x128_f8f6f4 v[68:71], v[16:23], v[222:229], v[68:71]
	v_mfma_f32_16x16x128_f8f6f4 v[52:55], v[16:23], v[230:237], v[52:55]
	v_mfma_f32_16x16x128_f8f6f4 v[44:47], v[24:31], v[230:237], v[44:47]
	v_mfma_f32_16x16x128_f8f6f4 v[32:35], v[24:31], v[238:245], v[32:35]
	v_mfma_f32_16x16x128_f8f6f4 v[36:39], v[16:23], v[238:245], v[36:39]
	s_setprio 0
	s_barrier
	s_add_i32 s62, s62, 2
	s_add_u32 s24, s24, 0x100
	s_addc_u32 s25, s25, 0
	s_cmp_gt_u32 s62, 29
	s_cbranch_scc1 .LBB0_1552
